# P7 drain loops: the last item of a wave's share no longer issues the pipelined reload of itself (16 dead loads per wave); skip path waits vmcnt(0)
# speedup vs baseline: 1.0195x; 1.0082x over previous
; __device__ __forceinline__ void t128_load(const float* W, int N, int item, int lane, f32x4 (&v)[16]) {
;     const int nblk = N / 32, kb = item / nblk, nb = item % nblk, k0 = 128 * kb, n0 = 32 * nb;
; #pragma unroll
;     for (int i = 0; i < 16; ++i) v[i] = __builtin_nontemporal_load((const f32x4*)(W + (size_t)(k0 + i * 8 + (lane >> 3)) * N + n0 + (lane & 7) * 4));
; }
; __device__ __forceinline__ void drain_balanced(const Ctx& c, const unsigned* ctl, const float* w_gu, const float* w_d, unsigned char* Wgu, unsigned char* Wd) {
;     ...
;         for (;;) {
;             { const int v2 = v + 1; const bool more = v2 < hi; const int it2 = more ? __builtin_amdgcn_readfirstlane(item_of(v2)) : it;
;               cs_load(it2, c.lane, w_gu, w_d, vb); cs_store(c, it, va, Wgu, Wd); v = v2; it = it2; if (!more) break; }
;             { const int v2 = v + 1; const bool more = v2 < hi; const int it2 = more ? __builtin_amdgcn_readfirstlane(item_of(v2)) : it;
;               cs_load(it2, c.lane, w_gu, w_d, va); cs_store(c, it, vb, Wgu, Wd); v = v2; it = it2; if (!more) break; }
;         }
.LBB0_1203:
	s_waitcnt vmcnt(4)
	v_or_b32_e32 v122, s8, v131
	v_lshlrev_b32_e32 v132, 2, v130
	v_ashrrev_i32_e32 v123, 31, v122
	v_lshl_add_u64 v[124:125], s[16:17], 0, v[132:133]
	v_lshlrev_b64 v[66:67], s14, v[122:123]
	v_lshl_add_u64 v[74:75], v[124:125], 0, v[66:67]
	v_add_u32_e32 v66, 8, v122
	v_ashrrev_i32_e32 v67, 31, v66
	v_lshlrev_b64 v[66:67], s14, v[66:67]
	v_lshl_add_u64 v[76:77], v[124:125], 0, v[66:67]
	s_and_b64 vcc, exec, s[12:13]
	s_cbranch_vccnz .Lcv7a_load
	s_waitcnt vmcnt(0)
	s_branch .Lcv7a_noload
.Lcv7a_load:
	global_load_dwordx4 v[70:73], v[74:75], off nt
	global_load_dwordx4 v[66:69], v[76:77], off nt
	v_add_u32_e32 v74, 16, v122
	v_ashrrev_i32_e32 v75, 31, v74
	v_lshlrev_b64 v[74:75], s14, v[74:75]
	v_lshl_add_u64 v[82:83], v[124:125], 0, v[74:75]
	v_add_u32_e32 v74, 24, v122
	v_ashrrev_i32_e32 v75, 31, v74
	v_lshlrev_b64 v[74:75], s14, v[74:75]
	v_lshl_add_u64 v[84:85], v[124:125], 0, v[74:75]
	global_load_dwordx4 v[78:81], v[82:83], off nt
	global_load_dwordx4 v[74:77], v[84:85], off nt
	v_add_u32_e32 v82, 32, v122
	v_ashrrev_i32_e32 v83, 31, v82
	v_lshlrev_b64 v[82:83], s14, v[82:83]
	v_lshl_add_u64 v[90:91], v[124:125], 0, v[82:83]
	v_add_u32_e32 v82, 40, v122
	v_ashrrev_i32_e32 v83, 31, v82
	v_lshlrev_b64 v[82:83], s14, v[82:83]
	v_lshl_add_u64 v[92:93], v[124:125], 0, v[82:83]
	global_load_dwordx4 v[86:89], v[90:91], off nt
	global_load_dwordx4 v[82:85], v[92:93], off nt
	v_add_u32_e32 v90, 48, v122
	v_ashrrev_i32_e32 v91, 31, v90
	v_lshlrev_b64 v[90:91], s14, v[90:91]
	v_lshl_add_u64 v[98:99], v[124:125], 0, v[90:91]
	v_add_u32_e32 v90, 56, v122
	v_ashrrev_i32_e32 v91, 31, v90
	v_lshlrev_b64 v[90:91], s14, v[90:91]
	v_lshl_add_u64 v[100:101], v[124:125], 0, v[90:91]
	global_load_dwordx4 v[94:97], v[98:99], off nt
	global_load_dwordx4 v[90:93], v[100:101], off nt
	v_add_u32_e32 v98, 64, v122
	v_add_u32_e32 v100, 0x48, v122
	v_add_u32_e32 v106, 0x50, v122
	v_add_u32_e32 v108, 0x58, v122
	v_add_u32_e32 v114, 0x60, v122
	v_add_u32_e32 v116, 0x68, v122
	v_add_u32_e32 v126, 0x70, v122
	v_add_u32_e32 v122, 0x78, v122
	v_ashrrev_i32_e32 v99, 31, v98
	v_ashrrev_i32_e32 v101, 31, v100
	v_ashrrev_i32_e32 v107, 31, v106
	v_ashrrev_i32_e32 v109, 31, v108
	v_ashrrev_i32_e32 v115, 31, v114
	v_ashrrev_i32_e32 v117, 31, v116
	v_ashrrev_i32_e32 v127, 31, v126
	v_ashrrev_i32_e32 v123, 31, v122
	v_lshlrev_b64 v[98:99], s14, v[98:99]
	v_lshlrev_b64 v[100:101], s14, v[100:101]
	v_lshlrev_b64 v[106:107], s14, v[106:107]
	v_lshlrev_b64 v[108:109], s14, v[108:109]
	v_lshlrev_b64 v[114:115], s14, v[114:115]
	v_lshlrev_b64 v[116:117], s14, v[116:117]
	v_lshlrev_b64 v[126:127], s14, v[126:127]
	v_lshlrev_b64 v[122:123], s14, v[122:123]
	v_lshl_add_u64 v[98:99], v[124:125], 0, v[98:99]
	v_lshl_add_u64 v[100:101], v[124:125], 0, v[100:101]
	v_lshl_add_u64 v[106:107], v[124:125], 0, v[106:107]
	v_lshl_add_u64 v[108:109], v[124:125], 0, v[108:109]
	v_lshl_add_u64 v[114:115], v[124:125], 0, v[114:115]
	v_lshl_add_u64 v[116:117], v[124:125], 0, v[116:117]
	v_lshl_add_u64 v[126:127], v[124:125], 0, v[126:127]
	v_lshl_add_u64 v[122:123], v[124:125], 0, v[122:123]
	global_load_dwordx4 v[102:105], v[98:99], off nt
	s_nop 0
	global_load_dwordx4 v[98:101], v[100:101], off nt
	s_nop 0
	global_load_dwordx4 v[110:113], v[106:107], off nt
	s_nop 0
	global_load_dwordx4 v[106:109], v[108:109], off nt
	s_nop 0
	global_load_dwordx4 v[118:121], v[114:115], off nt
	s_nop 0
	global_load_dwordx4 v[114:117], v[116:117], off nt
	s_nop 0
	global_load_dwordx4 v[126:129], v[126:127], off nt
	s_nop 0
	global_load_dwordx4 v[122:125], v[122:123], off nt
.Lcv7a_noload:
	s_mov_b64 s[14:15], -1
	s_cmpk_gt_i32 s24, 0x7fff
	v_add_u32_e32 v146, 0x1080, v136
	v_add_u32_e32 v147, 0x1088, v136
	v_add_u32_e32 v148, 0x14a0, v136
	v_add_u32_e32 v149, 0x14a8, v136
	v_add_u32_e32 v150, 0x18c0, v136
	v_add_u32_e32 v151, 0x18c8, v136
	v_add_u32_e32 v152, 0x1ce0, v136
	v_add_u32_e32 v153, 0x1ce8, v136
	v_add_u32_e32 v154, 0x2100, v136
	v_add_u32_e32 v155, 0x2108, v136
	v_add_u32_e32 v156, 0x2520, v136
	v_add_u32_e32 v157, 0x2528, v136
	v_add_u32_e32 v158, 0x2940, v136
	v_add_u32_e32 v159, 0x2948, v136
	v_add_u32_e32 v160, 0x2d60, v136
	v_add_u32_e32 v161, 0x2d68, v136
	v_add_u32_e32 v163, 0x3180, v136
	v_add_u32_e32 v164, 0x3188, v136
	v_add_u32_e32 v165, 0x35a0, v136
	v_add_u32_e32 v166, 0x35a8, v136
	v_add_u32_e32 v167, 0x39c0, v136
	v_add_u32_e32 v168, 0x39c8, v136
	v_add_u32_e32 v169, 0x3de0, v136
	v_add_u32_e32 v170, 0x3de8, v136
	v_add_u32_e32 v145, 0x400, v140
	v_add_u32_e32 v144, 0x600, v140
	s_cbranch_scc0 .LBB0_1205
; #define LAS __attribute__((address_space(3)))
; #define LDS_WAIT() asm volatile("s_waitcnt lgkmcnt(0)" ::: "memory")
; template <int MODE>
; __device__ __forceinline__ void t128_store(const Ctx& c, const f32x4 (&v)[16], int K, int N, unsigned char* WT, int item) {
;     LAS float* scr = (LAS float*)(c.lds + c.wave * CONV_SCR);
;     const int nblk = N / 32, kb = item / nblk, nb = item % nblk, k0 = 128 * kb, n0 = 32 * nb, lane = c.lane;
; #pragma unroll
;     for (int i = 0; i < 16; ++i) { LAS float* d = scr + (i * 8 + (lane >> 3)) * 33 + (lane & 7) * 4; d[0] = v[i].x; d[1] = v[i].y; d[2] = v[i].z; d[3] = v[i].w; }
;     LDS_WAIT(); asm volatile("" ::: "memory");
;     const int cc = lane & 7;
; #pragma unroll
;     for (int j = 0; j < 4; ++j) { const int n = (lane >> 3) + 8 * j; const LAS float* s = scr + (16 * cc) * 33 + n; int w[4];
; #pragma unroll
;         for (int q = 0; q < 4; ++q) { int t = 0; t = __builtin_amdgcn_cvt_pk_fp8_f32(s[(4 * q) * 33] * WSCALE, s[(4 * q + 1) * 33] * WSCALE, t, false);
;             t = __builtin_amdgcn_cvt_pk_fp8_f32(s[(4 * q + 2) * 33] * WSCALE, s[(4 * q + 3) * 33] * WSCALE, t, true); w[q] = t; }
;         const int dr = drow_of<MODE>(n0 + n);
;         __builtin_nontemporal_store((u32x4){(unsigned)w[0], (unsigned)w[1], (unsigned)w[2], (unsigned)w[3]}, (u32x4*)(WT + (size_t)dr * K + k0 + 16 * cc)); }
;     LDS_WAIT(); asm volatile("" ::: "memory");
; }
; __device__ __forceinline__ void cs_store(const Ctx& c, int it, const f32x4 (&v)[16], unsigned char* Wgu, unsigned char* Wd) {
;     if (it < I_D) { constexpr int per = (DFF / 128) * (D / 32); t128_store<0>(c, v, DFF, D, Wd + (size_t)(it / per) * D * DFF, it % per); }
;     else { const int r = it - I_D; constexpr int per = (D / 128) * (4096 / 32); t128_store<1>(c, v, D, 4096, Wgu + (size_t)(r / per) * 4096 * D, r % per); }
	s_waitcnt vmcnt(31)
	ds_write2_b32 v136, v6, v7 offset1:1
	ds_write2_b32 v136, v8, v9 offset0:2 offset1:3
	s_waitcnt vmcnt(30)
	ds_write2_b32 v141, v2, v3 offset1:1
	ds_write2_b32 v141, v4, v5 offset0:2 offset1:3
	s_waitcnt vmcnt(29)
	ds_write2_b32 v142, v14, v15 offset1:1
	ds_write2_b32 v142, v16, v17 offset0:2 offset1:3
	s_waitcnt vmcnt(28)
	ds_write2_b32 v143, v10, v11 offset1:1
	ds_write2_b32 v143, v12, v13 offset0:2 offset1:3
	s_waitcnt vmcnt(27)
	ds_write2_b32 v146, v22, v23 offset1:1
	ds_write2_b32 v147, v24, v25 offset1:1
	s_waitcnt vmcnt(26)
	ds_write2_b32 v148, v18, v19 offset1:1
	ds_write2_b32 v149, v20, v21 offset1:1
	s_waitcnt vmcnt(25)
	ds_write2_b32 v150, v30, v31 offset1:1
	ds_write2_b32 v151, v32, v33 offset1:1
	s_waitcnt vmcnt(24)
	ds_write2_b32 v152, v26, v27 offset1:1
	ds_write2_b32 v153, v28, v29 offset1:1
	s_waitcnt vmcnt(23)
	ds_write2_b32 v154, v38, v39 offset1:1
	ds_write2_b32 v155, v40, v41 offset1:1
	s_waitcnt vmcnt(22)
	ds_write2_b32 v156, v34, v35 offset1:1
	ds_write2_b32 v157, v36, v37 offset1:1
	s_waitcnt vmcnt(21)
	ds_write2_b32 v158, v46, v47 offset1:1
	ds_write2_b32 v159, v48, v49 offset1:1
	s_waitcnt vmcnt(20)
	ds_write2_b32 v160, v42, v43 offset1:1
	ds_write2_b32 v161, v44, v45 offset1:1
	s_waitcnt vmcnt(19)
	ds_write2_b32 v163, v54, v55 offset1:1
	ds_write2_b32 v164, v56, v57 offset1:1
	s_waitcnt vmcnt(18)
	ds_write2_b32 v165, v50, v51 offset1:1
	ds_write2_b32 v166, v52, v53 offset1:1
	s_waitcnt vmcnt(17)
	ds_write2_b32 v167, v62, v63 offset1:1
	ds_write2_b32 v168, v64, v65 offset1:1
	s_waitcnt vmcnt(16)
	ds_write2_b32 v169, v58, v59 offset1:1
	ds_write2_b32 v170, v60, v61 offset1:1
	s_waitcnt lgkmcnt(0)
	ds_read2_b32 v[176:177], v140 offset1:8
	ds_read2_b32 v[178:179], v140 offset0:33 offset1:41
	ds_read2_b32 v[182:183], v140 offset0:66 offset1:74
	ds_read2_b32 v[184:185], v140 offset0:99 offset1:107
	v_mov_b32_e32 v172, v133
	ds_read2_b32 v[186:187], v140 offset0:132 offset1:140
	ds_read2_b32 v[188:189], v140 offset0:165 offset1:173
	s_waitcnt lgkmcnt(5)
	v_mul_f32_e32 v171, 0x42800000, v176
	s_waitcnt lgkmcnt(4)
	v_mul_f32_e32 v173, 0x42800000, v178
	v_cvt_pk_fp8_f32 v172, v171, v173
	s_waitcnt lgkmcnt(3)
	v_mul_f32_e32 v171, 0x42800000, v182
	s_waitcnt lgkmcnt(2)
	v_mul_f32_e32 v173, 0x42800000, v184
	ds_read2_b32 v[190:191], v140 offset0:198 offset1:206
	ds_read2_b32 v[192:193], v140 offset0:231 offset1:239
	v_cvt_pk_fp8_f32 v172, v171, v173 op_sel:[0,0,1]
	s_waitcnt lgkmcnt(3)
	v_mul_f32_e32 v171, 0x42800000, v186
	s_waitcnt lgkmcnt(2)
	v_mul_f32_e32 v174, 0x42800000, v188
	v_mov_b32_e32 v173, v133
	ds_read2_b32 v[194:195], v145 offset0:8 offset1:16
	ds_read2_b32 v[196:197], v145 offset0:41 offset1:49
	v_cvt_pk_fp8_f32 v173, v171, v174
	ds_read2_b32 v[198:199], v145 offset0:74 offset1:82
	ds_read2_b32 v[200:201], v145 offset0:107 offset1:115
	ds_read2_b32 v[202:203], v145 offset0:140 offset1:148
	ds_read2_b32 v[204:205], v145 offset0:173 offset1:181
	s_add_i32 s8, s24, 0xffff8000
	s_lshr_b32 s8, s8, 11
	s_waitcnt lgkmcnt(7)
	v_mul_f32_e32 v171, 0x42800000, v190
	s_waitcnt lgkmcnt(6)
	v_mul_f32_e32 v174, 0x42800000, v192
	s_lshl_b64 s[14:15], s[8:9], 23
	v_cvt_pk_fp8_f32 v173, v171, v174 op_sel:[0,0,1]
	s_waitcnt lgkmcnt(5)
	v_mul_f32_e32 v171, 0x42800000, v194
	s_waitcnt lgkmcnt(4)
	v_mul_f32_e32 v175, 0x42800000, v196
	v_mov_b32_e32 v174, v133
	ds_read2_b32 v[206:207], v145 offset0:206 offset1:214
	ds_read2_b32 v[208:209], v145 offset0:239 offset1:247
	s_add_u32 s8, s52, s14
	v_cvt_pk_fp8_f32 v174, v171, v175
	s_waitcnt lgkmcnt(3)
	v_mul_f32_e32 v178, 0x42800000, v202
	s_waitcnt lgkmcnt(2)
	v_mul_f32_e32 v182, 0x42800000, v204
	v_mov_b32_e32 v175, v133
	s_addc_u32 s15, s53, s15
	s_lshl_b32 s16, s24, 5
	s_and_b32 s14, s24, 0x780
	v_cvt_pk_fp8_f32 v175, v178, v182
	s_add_u32 s14, s8, s14
	s_addc_u32 s15, s15, 0
	v_mul_f32_e32 v171, 0x42800000, v198
	v_mul_f32_e32 v176, 0x42800000, v200
	s_lshl_b32 s8, s24, 6
	v_lshl_add_u64 v[180:181], s[14:15], 0, v[134:135]
	v_cvt_pk_fp8_f32 v174, v171, v176 op_sel:[0,0,1]
	s_waitcnt lgkmcnt(1)
	v_mul_f32_e32 v171, 0x42800000, v206
	s_waitcnt lgkmcnt(0)
; #define LAS __attribute__((address_space(3)))
; #define LDS_WAIT() asm volatile("s_waitcnt lgkmcnt(0)" ::: "memory")
; template <int MODE>
; __device__ __forceinline__ void t128_store(const Ctx& c, const f32x4 (&v)[16], int K, int N, unsigned char* WT, int item) {
;     LAS float* scr = (LAS float*)(c.lds + c.wave * CONV_SCR);
;     const int nblk = N / 32, kb = item / nblk, nb = item % nblk, k0 = 128 * kb, n0 = 32 * nb, lane = c.lane;
; #pragma unroll
;     for (int i = 0; i < 16; ++i) { LAS float* d = scr + (i * 8 + (lane >> 3)) * 33 + (lane & 7) * 4; d[0] = v[i].x; d[1] = v[i].y; d[2] = v[i].z; d[3] = v[i].w; }
;     LDS_WAIT(); asm volatile("" ::: "memory");
;     const int cc = lane & 7;
; #pragma unroll
;     for (int j = 0; j < 4; ++j) { const int n = (lane >> 3) + 8 * j; const LAS float* s = scr + (16 * cc) * 33 + n; int w[4];
; #pragma unroll
;         for (int q = 0; q < 4; ++q) { int t = 0; t = __builtin_amdgcn_cvt_pk_fp8_f32(s[(4 * q) * 33] * WSCALE, s[(4 * q + 1) * 33] * WSCALE, t, false);
;             t = __builtin_amdgcn_cvt_pk_fp8_f32(s[(4 * q + 2) * 33] * WSCALE, s[(4 * q + 3) * 33] * WSCALE, t, true); w[q] = t; }
;         const int dr = drow_of<MODE>(n0 + n);
;         __builtin_nontemporal_store((u32x4){(unsigned)w[0], (unsigned)w[1], (unsigned)w[2], (unsigned)w[3]}, (u32x4*)(WT + (size_t)dr * K + k0 + 16 * cc)); }
;     LDS_WAIT(); asm volatile("" ::: "memory");
; }
; __device__ __forceinline__ void cs_store(const Ctx& c, int it, const f32x4 (&v)[16], unsigned char* Wgu, unsigned char* Wd) {
;     if (it < I_D) { constexpr int per = (DFF / 128) * (D / 32); t128_store<0>(c, v, DFF, D, Wd + (size_t)(it / per) * D * DFF, it % per); }
;     else { const int r = it - I_D; constexpr int per = (D / 128) * (4096 / 32); t128_store<1>(c, v, D, 4096, Wgu + (size_t)(r / per) * 4096 * D, r % per); }
	v_mul_f32_e32 v176, 0x42800000, v208
	s_and_b32 s8, s8, 0xf00
	s_lshl_b32 s14, s24, 1
	s_and_b32 s15, s16, 0x60
	v_cvt_pk_fp8_f32 v175, v171, v176 op_sel:[0,0,1]
	s_and_b32 s14, s14, 0x80
	s_or_b32 s8, s15, s8
	s_or_b32 s8, s8, s14
	v_add_lshl_u32 v210, s8, v131, 11
	v_mov_b32_e32 v211, v133
	v_lshl_add_u64 v[210:211], v[180:181], 0, v[210:211]
	global_store_dwordx4 v[210:211], v[172:175], off nt
	v_mul_f32_e32 v171, 0x42800000, v177
	v_mul_f32_e32 v176, 0x42800000, v189
	v_mul_f32_e32 v173, 0x42800000, v179
	v_mov_b32_e32 v172, v133
	v_cvt_pk_fp8_f32 v172, v171, v173
	v_mul_f32_e32 v175, 0x42800000, v187
	v_mov_b32_e32 v173, v133
	v_cvt_pk_fp8_f32 v173, v175, v176
	v_mul_f32_e32 v171, 0x42800000, v183
	v_mul_f32_e32 v174, 0x42800000, v185
	v_cvt_pk_fp8_f32 v172, v171, v174 op_sel:[0,0,1]
	v_mul_f32_e32 v171, 0x42800000, v191
	v_mul_f32_e32 v174, 0x42800000, v193
	v_cvt_pk_fp8_f32 v173, v171, v174 op_sel:[0,0,1]
	v_mul_f32_e32 v171, 0x42800000, v195
	v_mul_f32_e32 v175, 0x42800000, v197
	v_mov_b32_e32 v174, v133
	v_cvt_pk_fp8_f32 v174, v171, v175
	v_mul_f32_e32 v177, 0x42800000, v203
	v_mul_f32_e32 v178, 0x42800000, v205
	v_mov_b32_e32 v175, v133
	v_cvt_pk_fp8_f32 v175, v177, v178
	v_mul_f32_e32 v171, 0x42800000, v199
	v_mul_f32_e32 v176, 0x42800000, v201
	v_cvt_pk_fp8_f32 v174, v171, v176 op_sel:[0,0,1]
	v_mul_f32_e32 v171, 0x42800000, v207
	v_mul_f32_e32 v176, 0x42800000, v209
	v_cvt_pk_fp8_f32 v175, v171, v176 op_sel:[0,0,1]
	ds_read2_b32 v[178:179], v140 offset0:16 offset1:24
	ds_read2_b32 v[182:183], v140 offset0:49 offset1:57
	v_add_lshl_u32 v176, s8, v137, 11
	v_mov_b32_e32 v177, v133
	v_lshl_add_u64 v[176:177], v[180:181], 0, v[176:177]
	global_store_dwordx4 v[176:177], v[172:175], off nt
	ds_read2_b32 v[176:177], v140 offset0:82 offset1:90
	ds_read2_b32 v[184:185], v140 offset0:115 offset1:123
	s_waitcnt lgkmcnt(3)
	v_mul_f32_e32 v171, 0x42800000, v178
	s_waitcnt lgkmcnt(2)
	v_mul_f32_e32 v173, 0x42800000, v182
	v_mov_b32_e32 v172, v133
	ds_read2_b32 v[186:187], v140 offset0:148 offset1:156
	ds_read2_b32 v[188:189], v140 offset0:181 offset1:189
	v_cvt_pk_fp8_f32 v172, v171, v173
	s_waitcnt lgkmcnt(3)
	v_mul_f32_e32 v171, 0x42800000, v176
	s_waitcnt lgkmcnt(2)
	v_mul_f32_e32 v173, 0x42800000, v184
	ds_read2_b32 v[190:191], v140 offset0:214 offset1:222
	ds_read2_b32 v[192:193], v140 offset0:247 offset1:255
	v_cvt_pk_fp8_f32 v172, v171, v173 op_sel:[0,0,1]
	s_waitcnt lgkmcnt(3)
	v_mul_f32_e32 v171, 0x42800000, v186
	s_waitcnt lgkmcnt(2)
	v_mul_f32_e32 v174, 0x42800000, v188
	v_mov_b32_e32 v173, v133
	ds_read2_b32 v[194:195], v145 offset0:24 offset1:32
	ds_read2_b32 v[196:197], v145 offset0:57 offset1:65
	v_cvt_pk_fp8_f32 v173, v171, v174
	ds_read2_b32 v[198:199], v145 offset0:90 offset1:98
	ds_read2_b32 v[200:201], v145 offset0:123 offset1:131
	ds_read2_b32 v[202:203], v145 offset0:156 offset1:164
	ds_read2_b32 v[204:205], v145 offset0:189 offset1:197
	s_waitcnt lgkmcnt(7)
	v_mul_f32_e32 v171, 0x42800000, v190
	s_waitcnt lgkmcnt(6)
	v_mul_f32_e32 v174, 0x42800000, v192
	v_cvt_pk_fp8_f32 v173, v171, v174 op_sel:[0,0,1]
	s_waitcnt lgkmcnt(5)
	v_mul_f32_e32 v171, 0x42800000, v194
	s_waitcnt lgkmcnt(4)
	v_mul_f32_e32 v175, 0x42800000, v196
	v_mov_b32_e32 v174, v133
	ds_read2_b32 v[206:207], v145 offset0:222 offset1:230
	ds_read2_b32 v[208:209], v144 offset0:127 offset1:135
	v_cvt_pk_fp8_f32 v174, v171, v175
	s_waitcnt lgkmcnt(3)
	v_mul_f32_e32 v178, 0x42800000, v202
	s_waitcnt lgkmcnt(2)
	v_mul_f32_e32 v182, 0x42800000, v204
	v_mov_b32_e32 v175, v133
	v_cvt_pk_fp8_f32 v175, v178, v182
	v_mul_f32_e32 v171, 0x42800000, v198
	v_mul_f32_e32 v176, 0x42800000, v200
	v_cvt_pk_fp8_f32 v174, v171, v176 op_sel:[0,0,1]
	s_waitcnt lgkmcnt(1)
	v_mul_f32_e32 v171, 0x42800000, v206
	s_waitcnt lgkmcnt(0)
	v_mul_f32_e32 v176, 0x42800000, v208
	v_cvt_pk_fp8_f32 v175, v171, v176 op_sel:[0,0,1]
	v_add_lshl_u32 v210, s8, v138, 11
	v_mov_b32_e32 v211, v133
	v_lshl_add_u64 v[210:211], v[180:181], 0, v[210:211]
	global_store_dwordx4 v[210:211], v[172:175], off nt
	v_mul_f32_e32 v171, 0x42800000, v179
	v_mul_f32_e32 v176, 0x42800000, v189
	v_mul_f32_e32 v173, 0x42800000, v183
	v_mov_b32_e32 v172, v133
	v_cvt_pk_fp8_f32 v172, v171, v173
	v_mul_f32_e32 v175, 0x42800000, v187
	v_mov_b32_e32 v173, v133
	v_cvt_pk_fp8_f32 v173, v175, v176
	v_mul_f32_e32 v171, 0x42800000, v177
	v_mul_f32_e32 v174, 0x42800000, v185
	v_cvt_pk_fp8_f32 v172, v171, v174 op_sel:[0,0,1]
	v_mul_f32_e32 v171, 0x42800000, v191
	v_mul_f32_e32 v174, 0x42800000, v193
	v_cvt_pk_fp8_f32 v173, v171, v174 op_sel:[0,0,1]
	v_mul_f32_e32 v171, 0x42800000, v195
	v_mul_f32_e32 v175, 0x42800000, v197
	v_mov_b32_e32 v174, v133
	v_cvt_pk_fp8_f32 v174, v171, v175
	v_mul_f32_e32 v177, 0x42800000, v203
	v_mul_f32_e32 v178, 0x42800000, v205
	v_mov_b32_e32 v175, v133
	v_cvt_pk_fp8_f32 v175, v177, v178
	v_mul_f32_e32 v171, 0x42800000, v199
	v_mul_f32_e32 v176, 0x42800000, v201
	v_cvt_pk_fp8_f32 v174, v171, v176 op_sel:[0,0,1]
	v_mul_f32_e32 v171, 0x42800000, v207
	v_mul_f32_e32 v176, 0x42800000, v209
	v_cvt_pk_fp8_f32 v175, v171, v176 op_sel:[0,0,1]
	v_add_lshl_u32 v176, s8, v139, 11
	v_mov_b32_e32 v177, v133
	v_lshl_add_u64 v[176:177], v[180:181], 0, v[176:177]
	global_store_dwordx4 v[176:177], v[172:175], off nt
	s_waitcnt lgkmcnt(0)
	s_cbranch_execnz .LBB0_1207
	s_branch .LBB0_1206

; __device__ __forceinline__ void t128_load(const float* W, int N, int item, int lane, f32x4 (&v)[16]) {
;     const int nblk = N / 32, kb = item / nblk, nb = item % nblk, k0 = 128 * kb, n0 = 32 * nb;
; #pragma unroll
;     for (int i = 0; i < 16; ++i) v[i] = __builtin_nontemporal_load((const f32x4*)(W + (size_t)(k0 + i * 8 + (lane >> 3)) * N + n0 + (lane & 7) * 4));
; }
; __device__ __forceinline__ void drain_balanced(const Ctx& c, const unsigned* ctl, const float* w_gu, const float* w_d, unsigned char* Wgu, unsigned char* Wd) {
;     ...
;             { const int v2 = v + 1; const bool more = v2 < hi; const int it2 = more ? __builtin_amdgcn_readfirstlane(item_of(v2)) : it;
;               cs_load(it2, c.lane, w_gu, w_d, va); cs_store(c, it, vb, Wgu, Wd); v = v2; it = it2; if (!more) break; }
.LBB0_1217:
	s_waitcnt vmcnt(16)
	v_or_b32_e32 v58, s8, v131
	v_ashrrev_i32_e32 v59, 31, v58
	v_lshl_add_u64 v[60:61], s[16:17], 0, v[132:133]
	v_lshlrev_b64 v[2:3], s14, v[58:59]
	v_lshl_add_u64 v[10:11], v[60:61], 0, v[2:3]
	v_add_u32_e32 v2, 8, v58
	v_ashrrev_i32_e32 v3, 31, v2
	v_lshlrev_b64 v[2:3], s14, v[2:3]
	v_lshl_add_u64 v[12:13], v[60:61], 0, v[2:3]
	s_and_b64 vcc, exec, s[12:13]
	s_cbranch_vccz .Lcv7b_load
	s_waitcnt vmcnt(0)
	s_branch .Lcv7b_noload
.Lcv7b_load:
	global_load_dwordx4 v[6:9], v[10:11], off nt
	global_load_dwordx4 v[2:5], v[12:13], off nt
	v_add_u32_e32 v10, 16, v58
	v_add_u32_e32 v12, 24, v58
	v_add_u32_e32 v18, 32, v58
	v_add_u32_e32 v20, 40, v58
	v_add_u32_e32 v26, 48, v58
	v_add_u32_e32 v28, 56, v58
	v_add_u32_e32 v34, 64, v58
	v_add_u32_e32 v36, 0x48, v58
	v_add_u32_e32 v42, 0x50, v58
	v_add_u32_e32 v44, 0x58, v58
	v_add_u32_e32 v50, 0x60, v58
	v_add_u32_e32 v52, 0x68, v58
	v_add_u32_e32 v62, 0x70, v58
	v_add_u32_e32 v58, 0x78, v58
	v_ashrrev_i32_e32 v11, 31, v10
	v_ashrrev_i32_e32 v13, 31, v12
	v_ashrrev_i32_e32 v19, 31, v18
	v_ashrrev_i32_e32 v21, 31, v20
	v_ashrrev_i32_e32 v27, 31, v26
	v_ashrrev_i32_e32 v29, 31, v28
	v_ashrrev_i32_e32 v35, 31, v34
	v_ashrrev_i32_e32 v37, 31, v36
	v_ashrrev_i32_e32 v43, 31, v42
	v_ashrrev_i32_e32 v45, 31, v44
	v_ashrrev_i32_e32 v51, 31, v50
	v_ashrrev_i32_e32 v53, 31, v52
	v_ashrrev_i32_e32 v63, 31, v62
	v_ashrrev_i32_e32 v59, 31, v58
	v_lshlrev_b64 v[10:11], s14, v[10:11]
	v_lshlrev_b64 v[12:13], s14, v[12:13]
	v_lshlrev_b64 v[18:19], s14, v[18:19]
	v_lshlrev_b64 v[20:21], s14, v[20:21]
	v_lshlrev_b64 v[26:27], s14, v[26:27]
	v_lshlrev_b64 v[28:29], s14, v[28:29]
	v_lshlrev_b64 v[34:35], s14, v[34:35]
	v_lshlrev_b64 v[36:37], s14, v[36:37]
	v_lshlrev_b64 v[42:43], s14, v[42:43]
	v_lshlrev_b64 v[44:45], s14, v[44:45]
	v_lshlrev_b64 v[50:51], s14, v[50:51]
	v_lshlrev_b64 v[52:53], s14, v[52:53]
	v_lshlrev_b64 v[62:63], s14, v[62:63]
	v_lshlrev_b64 v[58:59], s14, v[58:59]
	v_lshl_add_u64 v[10:11], v[60:61], 0, v[10:11]
	v_lshl_add_u64 v[12:13], v[60:61], 0, v[12:13]
	v_lshl_add_u64 v[18:19], v[60:61], 0, v[18:19]
	v_lshl_add_u64 v[20:21], v[60:61], 0, v[20:21]
	v_lshl_add_u64 v[26:27], v[60:61], 0, v[26:27]
	v_lshl_add_u64 v[28:29], v[60:61], 0, v[28:29]
	v_lshl_add_u64 v[34:35], v[60:61], 0, v[34:35]
	v_lshl_add_u64 v[36:37], v[60:61], 0, v[36:37]
	v_lshl_add_u64 v[42:43], v[60:61], 0, v[42:43]
	v_lshl_add_u64 v[44:45], v[60:61], 0, v[44:45]
	v_lshl_add_u64 v[50:51], v[60:61], 0, v[50:51]
	v_lshl_add_u64 v[52:53], v[60:61], 0, v[52:53]
	v_lshl_add_u64 v[62:63], v[60:61], 0, v[62:63]
	v_lshl_add_u64 v[58:59], v[60:61], 0, v[58:59]
	global_load_dwordx4 v[14:17], v[10:11], off nt
	s_nop 0
	global_load_dwordx4 v[10:13], v[12:13], off nt
	s_nop 0
	global_load_dwordx4 v[22:25], v[18:19], off nt
	s_nop 0
	global_load_dwordx4 v[18:21], v[20:21], off nt
	s_nop 0
	global_load_dwordx4 v[30:33], v[26:27], off nt
	s_nop 0
	global_load_dwordx4 v[26:29], v[28:29], off nt
	s_nop 0
	global_load_dwordx4 v[38:41], v[34:35], off nt
	s_nop 0
	global_load_dwordx4 v[34:37], v[36:37], off nt
	s_nop 0
	global_load_dwordx4 v[46:49], v[42:43], off nt
	s_nop 0
	global_load_dwordx4 v[42:45], v[44:45], off nt
	s_nop 0
	global_load_dwordx4 v[54:57], v[50:51], off nt
	s_nop 0
	global_load_dwordx4 v[50:53], v[52:53], off nt
	s_nop 0
	global_load_dwordx4 v[62:65], v[62:63], off nt
	s_nop 0
	global_load_dwordx4 v[58:61], v[58:59], off nt
.Lcv7b_noload:
	s_mov_b64 s[14:15], -1
	s_and_b64 vcc, exec, s[10:11]
	s_cbranch_vccz .LBB0_1219
	s_waitcnt vmcnt(31)
	ds_write2_b32 v136, v70, v71 offset1:1
	ds_write2_b32 v136, v72, v73 offset0:2 offset1:3
	s_waitcnt vmcnt(30)
	ds_write2_b32 v141, v66, v67 offset1:1
	ds_write2_b32 v141, v68, v69 offset0:2 offset1:3
	s_waitcnt vmcnt(29)
	ds_write2_b32 v142, v78, v79 offset1:1
	ds_write2_b32 v142, v80, v81 offset0:2 offset1:3
	s_waitcnt vmcnt(28)
	ds_write2_b32 v143, v74, v75 offset1:1
	ds_write2_b32 v143, v76, v77 offset0:2 offset1:3
	s_waitcnt vmcnt(27)
	ds_write2_b32 v146, v86, v87 offset1:1
	ds_write2_b32 v147, v88, v89 offset1:1
	s_waitcnt vmcnt(26)
	ds_write2_b32 v148, v82, v83 offset1:1
	ds_write2_b32 v149, v84, v85 offset1:1
	s_waitcnt vmcnt(25)
	ds_write2_b32 v150, v94, v95 offset1:1
	ds_write2_b32 v151, v96, v97 offset1:1
	s_waitcnt vmcnt(24)
	ds_write2_b32 v152, v90, v91 offset1:1
	ds_write2_b32 v153, v92, v93 offset1:1
	s_waitcnt vmcnt(23)
	ds_write2_b32 v154, v102, v103 offset1:1
	ds_write2_b32 v155, v104, v105 offset1:1
	s_waitcnt vmcnt(22)
	ds_write2_b32 v156, v98, v99 offset1:1
	ds_write2_b32 v157, v100, v101 offset1:1
	s_waitcnt vmcnt(21)
	ds_write2_b32 v158, v110, v111 offset1:1
	ds_write2_b32 v159, v112, v113 offset1:1
	s_waitcnt vmcnt(20)
	ds_write2_b32 v160, v106, v107 offset1:1
	ds_write2_b32 v161, v108, v109 offset1:1
	s_waitcnt vmcnt(19)
	ds_write2_b32 v163, v118, v119 offset1:1
	ds_write2_b32 v164, v120, v121 offset1:1
	s_waitcnt vmcnt(18)
	ds_write2_b32 v165, v114, v115 offset1:1
	ds_write2_b32 v166, v116, v117 offset1:1
	s_waitcnt vmcnt(17)
	ds_write2_b32 v167, v126, v127 offset1:1
	ds_write2_b32 v168, v128, v129 offset1:1
	s_waitcnt vmcnt(16)
	ds_write2_b32 v169, v122, v123 offset1:1
	ds_write2_b32 v170, v124, v125 offset1:1
	s_waitcnt lgkmcnt(0)
	ds_read2_b32 v[176:177], v140 offset1:8
	ds_read2_b32 v[178:179], v140 offset0:33 offset1:41
	ds_read2_b32 v[182:183], v140 offset0:66 offset1:74
	ds_read2_b32 v[184:185], v140 offset0:99 offset1:107
	v_mov_b32_e32 v172, v133
	ds_read2_b32 v[186:187], v140 offset0:132 offset1:140
	ds_read2_b32 v[188:189], v140 offset0:165 offset1:173
	s_waitcnt lgkmcnt(5)
	v_mul_f32_e32 v132, 0x42800000, v176
	s_waitcnt lgkmcnt(4)
; #define LAS __attribute__((address_space(3)))
; #define LDS_WAIT() asm volatile("s_waitcnt lgkmcnt(0)" ::: "memory")
; template <int MODE>
; __device__ __forceinline__ void t128_store(const Ctx& c, const f32x4 (&v)[16], int K, int N, unsigned char* WT, int item) {
;     LAS float* scr = (LAS float*)(c.lds + c.wave * CONV_SCR);
;     const int nblk = N / 32, kb = item / nblk, nb = item % nblk, k0 = 128 * kb, n0 = 32 * nb, lane = c.lane;
; #pragma unroll
;     for (int i = 0; i < 16; ++i) { LAS float* d = scr + (i * 8 + (lane >> 3)) * 33 + (lane & 7) * 4; d[0] = v[i].x; d[1] = v[i].y; d[2] = v[i].z; d[3] = v[i].w; }
;     LDS_WAIT(); asm volatile("" ::: "memory");
;     const int cc = lane & 7;
; #pragma unroll
;     for (int j = 0; j < 4; ++j) { const int n = (lane >> 3) + 8 * j; const LAS float* s = scr + (16 * cc) * 33 + n; int w[4];
; #pragma unroll
;         for (int q = 0; q < 4; ++q) { int t = 0; t = __builtin_amdgcn_cvt_pk_fp8_f32(s[(4 * q) * 33] * WSCALE, s[(4 * q + 1) * 33] * WSCALE, t, false);
;             t = __builtin_amdgcn_cvt_pk_fp8_f32(s[(4 * q + 2) * 33] * WSCALE, s[(4 * q + 3) * 33] * WSCALE, t, true); w[q] = t; }
;         const int dr = drow_of<MODE>(n0 + n);
;         __builtin_nontemporal_store((u32x4){(unsigned)w[0], (unsigned)w[1], (unsigned)w[2], (unsigned)w[3]}, (u32x4*)(WT + (size_t)dr * K + k0 + 16 * cc)); }
;     LDS_WAIT(); asm volatile("" ::: "memory");
; }
; __device__ __forceinline__ void cs_store(const Ctx& c, int it, const f32x4 (&v)[16], unsigned char* Wgu, unsigned char* Wd) {
;     if (it < I_D) { constexpr int per = (DFF / 128) * (D / 32); t128_store<0>(c, v, DFF, D, Wd + (size_t)(it / per) * D * DFF, it % per); }
;     else { const int r = it - I_D; constexpr int per = (D / 128) * (4096 / 32); t128_store<1>(c, v, D, 4096, Wgu + (size_t)(r / per) * 4096 * D, r % per); }
	v_mul_f32_e32 v171, 0x42800000, v178
	v_cvt_pk_fp8_f32 v172, v132, v171
	s_waitcnt lgkmcnt(3)
	v_mul_f32_e32 v132, 0x42800000, v182
	s_waitcnt lgkmcnt(2)
	v_mul_f32_e32 v171, 0x42800000, v184
	ds_read2_b32 v[190:191], v140 offset0:198 offset1:206
	ds_read2_b32 v[192:193], v140 offset0:231 offset1:239
	v_cvt_pk_fp8_f32 v172, v132, v171 op_sel:[0,0,1]
	s_waitcnt lgkmcnt(3)
	v_mul_f32_e32 v132, 0x42800000, v186
	s_waitcnt lgkmcnt(2)
	v_mul_f32_e32 v171, 0x42800000, v188
	v_mov_b32_e32 v173, v133
	ds_read2_b32 v[194:195], v145 offset0:8 offset1:16
	ds_read2_b32 v[196:197], v145 offset0:41 offset1:49
	v_cvt_pk_fp8_f32 v173, v132, v171
	ds_read2_b32 v[198:199], v145 offset0:74 offset1:82
	ds_read2_b32 v[200:201], v145 offset0:107 offset1:115
	ds_read2_b32 v[202:203], v145 offset0:140 offset1:148
	ds_read2_b32 v[204:205], v145 offset0:173 offset1:181
	s_add_i32 s8, s25, 0xffff8000
	s_lshr_b32 s8, s8, 11
	s_waitcnt lgkmcnt(7)
	v_mul_f32_e32 v132, 0x42800000, v190
	s_waitcnt lgkmcnt(6)
	v_mul_f32_e32 v171, 0x42800000, v192
	s_lshl_b64 s[10:11], s[8:9], 23
	v_cvt_pk_fp8_f32 v173, v132, v171 op_sel:[0,0,1]
	s_waitcnt lgkmcnt(5)
	v_mul_f32_e32 v132, 0x42800000, v194
	s_waitcnt lgkmcnt(4)
	v_mul_f32_e32 v171, 0x42800000, v196
	v_mov_b32_e32 v174, v133
	ds_read2_b32 v[206:207], v145 offset0:206 offset1:214
	ds_read2_b32 v[208:209], v145 offset0:239 offset1:247
	s_add_u32 s8, s52, s10
	v_cvt_pk_fp8_f32 v174, v132, v171
	s_waitcnt lgkmcnt(3)
	v_mul_f32_e32 v176, 0x42800000, v202
	s_waitcnt lgkmcnt(2)
	v_mul_f32_e32 v178, 0x42800000, v204
	v_mov_b32_e32 v175, v133
	s_addc_u32 s11, s53, s11
	s_lshl_b32 s14, s25, 5
	s_and_b32 s10, s25, 0x780
	v_cvt_pk_fp8_f32 v175, v176, v178
	s_add_u32 s10, s8, s10
	s_addc_u32 s11, s11, 0
	v_mul_f32_e32 v132, 0x42800000, v198
	v_mul_f32_e32 v171, 0x42800000, v200
	s_lshl_b32 s8, s25, 6
	v_lshl_add_u64 v[180:181], s[10:11], 0, v[134:135]
	v_cvt_pk_fp8_f32 v174, v132, v171 op_sel:[0,0,1]
	s_waitcnt lgkmcnt(1)
	v_mul_f32_e32 v132, 0x42800000, v206
	s_waitcnt lgkmcnt(0)
	v_mul_f32_e32 v171, 0x42800000, v208
	s_and_b32 s8, s8, 0xf00
	s_lshl_b32 s10, s25, 1
	s_and_b32 s11, s14, 0x60
	v_cvt_pk_fp8_f32 v175, v132, v171 op_sel:[0,0,1]
	s_and_b32 s10, s10, 0x80
	s_or_b32 s8, s11, s8
	s_or_b32 s8, s8, s10
	v_add_lshl_u32 v132, s8, v131, 11
	v_lshl_add_u64 v[210:211], v[180:181], 0, v[132:133]
	global_store_dwordx4 v[210:211], v[172:175], off nt
	v_mul_f32_e32 v132, 0x42800000, v177
	v_mul_f32_e32 v171, 0x42800000, v179
	v_mov_b32_e32 v172, v133
	v_cvt_pk_fp8_f32 v172, v132, v171
	v_mul_f32_e32 v174, 0x42800000, v187
	v_mul_f32_e32 v175, 0x42800000, v189
	v_mov_b32_e32 v173, v133
	v_cvt_pk_fp8_f32 v173, v174, v175
	v_mul_f32_e32 v132, 0x42800000, v183
	v_mul_f32_e32 v171, 0x42800000, v185
	v_cvt_pk_fp8_f32 v172, v132, v171 op_sel:[0,0,1]
	v_mul_f32_e32 v132, 0x42800000, v191
	v_mul_f32_e32 v171, 0x42800000, v193
	v_cvt_pk_fp8_f32 v173, v132, v171 op_sel:[0,0,1]
	v_mul_f32_e32 v132, 0x42800000, v195
	v_mul_f32_e32 v171, 0x42800000, v197
	v_mov_b32_e32 v174, v133
	v_cvt_pk_fp8_f32 v174, v132, v171
	v_mul_f32_e32 v176, 0x42800000, v203
	v_mul_f32_e32 v177, 0x42800000, v205
	v_mov_b32_e32 v175, v133
	v_cvt_pk_fp8_f32 v175, v176, v177
	v_mul_f32_e32 v132, 0x42800000, v199
	v_mul_f32_e32 v171, 0x42800000, v201
	v_cvt_pk_fp8_f32 v174, v132, v171 op_sel:[0,0,1]
	v_mul_f32_e32 v132, 0x42800000, v207
	v_mul_f32_e32 v171, 0x42800000, v209
	v_cvt_pk_fp8_f32 v175, v132, v171 op_sel:[0,0,1]
	ds_read2_b32 v[176:177], v140 offset0:16 offset1:24
	ds_read2_b32 v[178:179], v140 offset0:49 offset1:57
	v_add_lshl_u32 v132, s8, v137, 11
	v_lshl_add_u64 v[182:183], v[180:181], 0, v[132:133]
	global_store_dwordx4 v[182:183], v[172:175], off nt
	ds_read2_b32 v[182:183], v140 offset0:82 offset1:90
	ds_read2_b32 v[184:185], v140 offset0:115 offset1:123
	s_waitcnt lgkmcnt(3)
; #define LAS __attribute__((address_space(3)))
; #define LDS_WAIT() asm volatile("s_waitcnt lgkmcnt(0)" ::: "memory")
; template <int MODE>
; __device__ __forceinline__ void t128_store(const Ctx& c, const f32x4 (&v)[16], int K, int N, unsigned char* WT, int item) {
;     LAS float* scr = (LAS float*)(c.lds + c.wave * CONV_SCR);
;     const int nblk = N / 32, kb = item / nblk, nb = item % nblk, k0 = 128 * kb, n0 = 32 * nb, lane = c.lane;
; #pragma unroll
;     for (int i = 0; i < 16; ++i) { LAS float* d = scr + (i * 8 + (lane >> 3)) * 33 + (lane & 7) * 4; d[0] = v[i].x; d[1] = v[i].y; d[2] = v[i].z; d[3] = v[i].w; }
;     LDS_WAIT(); asm volatile("" ::: "memory");
;     const int cc = lane & 7;
; #pragma unroll
;     for (int j = 0; j < 4; ++j) { const int n = (lane >> 3) + 8 * j; const LAS float* s = scr + (16 * cc) * 33 + n; int w[4];
; #pragma unroll
;         for (int q = 0; q < 4; ++q) { int t = 0; t = __builtin_amdgcn_cvt_pk_fp8_f32(s[(4 * q) * 33] * WSCALE, s[(4 * q + 1) * 33] * WSCALE, t, false);
;             t = __builtin_amdgcn_cvt_pk_fp8_f32(s[(4 * q + 2) * 33] * WSCALE, s[(4 * q + 3) * 33] * WSCALE, t, true); w[q] = t; }
;         const int dr = drow_of<MODE>(n0 + n);
;         __builtin_nontemporal_store((u32x4){(unsigned)w[0], (unsigned)w[1], (unsigned)w[2], (unsigned)w[3]}, (u32x4*)(WT + (size_t)dr * K + k0 + 16 * cc)); }
;     LDS_WAIT(); asm volatile("" ::: "memory");
; }
; __device__ __forceinline__ void cs_store(const Ctx& c, int it, const f32x4 (&v)[16], unsigned char* Wgu, unsigned char* Wd) {
;     if (it < I_D) { constexpr int per = (DFF / 128) * (D / 32); t128_store<0>(c, v, DFF, D, Wd + (size_t)(it / per) * D * DFF, it % per); }
;     else { const int r = it - I_D; constexpr int per = (D / 128) * (4096 / 32); t128_store<1>(c, v, D, 4096, Wgu + (size_t)(r / per) * 4096 * D, r % per); }
	v_mul_f32_e32 v132, 0x42800000, v176
	s_waitcnt lgkmcnt(2)
	v_mul_f32_e32 v171, 0x42800000, v178
	v_mov_b32_e32 v172, v133
	ds_read2_b32 v[186:187], v140 offset0:148 offset1:156
	ds_read2_b32 v[188:189], v140 offset0:181 offset1:189
	v_cvt_pk_fp8_f32 v172, v132, v171
	s_waitcnt lgkmcnt(3)
	v_mul_f32_e32 v132, 0x42800000, v182
	s_waitcnt lgkmcnt(2)
	v_mul_f32_e32 v171, 0x42800000, v184
	ds_read2_b32 v[190:191], v140 offset0:214 offset1:222
	ds_read2_b32 v[192:193], v140 offset0:247 offset1:255
	v_cvt_pk_fp8_f32 v172, v132, v171 op_sel:[0,0,1]
	s_waitcnt lgkmcnt(3)
	v_mul_f32_e32 v132, 0x42800000, v186
	s_waitcnt lgkmcnt(2)
	v_mul_f32_e32 v171, 0x42800000, v188
	v_mov_b32_e32 v173, v133
	ds_read2_b32 v[194:195], v145 offset0:24 offset1:32
	ds_read2_b32 v[196:197], v145 offset0:57 offset1:65
	v_cvt_pk_fp8_f32 v173, v132, v171
	ds_read2_b32 v[198:199], v145 offset0:90 offset1:98
	ds_read2_b32 v[200:201], v145 offset0:123 offset1:131
	ds_read2_b32 v[202:203], v145 offset0:156 offset1:164
	ds_read2_b32 v[204:205], v145 offset0:189 offset1:197
	s_waitcnt lgkmcnt(7)
	v_mul_f32_e32 v132, 0x42800000, v190
	s_waitcnt lgkmcnt(6)
	v_mul_f32_e32 v171, 0x42800000, v192
	v_cvt_pk_fp8_f32 v173, v132, v171 op_sel:[0,0,1]
	s_waitcnt lgkmcnt(5)
	v_mul_f32_e32 v132, 0x42800000, v194
	s_waitcnt lgkmcnt(4)
	v_mul_f32_e32 v171, 0x42800000, v196
	v_mov_b32_e32 v174, v133
	ds_read2_b32 v[206:207], v145 offset0:222 offset1:230
	ds_read2_b32 v[208:209], v144 offset0:127 offset1:135
	v_cvt_pk_fp8_f32 v174, v132, v171
	s_waitcnt lgkmcnt(3)
	v_mul_f32_e32 v176, 0x42800000, v202
	s_waitcnt lgkmcnt(2)
	v_mul_f32_e32 v178, 0x42800000, v204
	v_mov_b32_e32 v175, v133
	v_cvt_pk_fp8_f32 v175, v176, v178
	v_mul_f32_e32 v132, 0x42800000, v198
	v_mul_f32_e32 v171, 0x42800000, v200
	v_cvt_pk_fp8_f32 v174, v132, v171 op_sel:[0,0,1]
	s_waitcnt lgkmcnt(1)
	v_mul_f32_e32 v132, 0x42800000, v206
	s_waitcnt lgkmcnt(0)
	v_mul_f32_e32 v171, 0x42800000, v208
	v_cvt_pk_fp8_f32 v175, v132, v171 op_sel:[0,0,1]
	v_add_lshl_u32 v132, s8, v138, 11
	v_lshl_add_u64 v[210:211], v[180:181], 0, v[132:133]
	v_mul_f32_e32 v132, 0x42800000, v177
	v_mul_f32_e32 v171, 0x42800000, v179
	v_mov_b32_e32 v176, v133
	v_cvt_pk_fp8_f32 v176, v132, v171
	v_mul_f32_e32 v178, 0x42800000, v187
	v_mul_f32_e32 v179, 0x42800000, v189
	v_mov_b32_e32 v177, v133
	v_cvt_pk_fp8_f32 v177, v178, v179
	v_mul_f32_e32 v132, 0x42800000, v183
	v_mul_f32_e32 v171, 0x42800000, v185
	v_cvt_pk_fp8_f32 v176, v132, v171 op_sel:[0,0,1]
	v_mul_f32_e32 v132, 0x42800000, v191
	v_mul_f32_e32 v171, 0x42800000, v193
	v_cvt_pk_fp8_f32 v177, v132, v171 op_sel:[0,0,1]
	v_mul_f32_e32 v132, 0x42800000, v195
	v_mul_f32_e32 v171, 0x42800000, v197
	v_mov_b32_e32 v178, v133
	v_cvt_pk_fp8_f32 v178, v132, v171
	v_mul_f32_e32 v182, 0x42800000, v203
	v_mul_f32_e32 v183, 0x42800000, v205
	v_mov_b32_e32 v179, v133
	v_cvt_pk_fp8_f32 v179, v182, v183
	v_mul_f32_e32 v132, 0x42800000, v199
	v_mul_f32_e32 v171, 0x42800000, v201
	v_cvt_pk_fp8_f32 v178, v132, v171 op_sel:[0,0,1]
	v_mul_f32_e32 v132, 0x42800000, v207
	v_mul_f32_e32 v171, 0x42800000, v209
	v_cvt_pk_fp8_f32 v179, v132, v171 op_sel:[0,0,1]
	v_add_lshl_u32 v132, s8, v139, 11
	global_store_dwordx4 v[210:211], v[172:175], off nt
	s_mov_b64 s[14:15], 0
	s_nop 0
	v_lshl_add_u64 v[172:173], v[180:181], 0, v[132:133]
	global_store_dwordx4 v[172:173], v[176:179], off nt
	s_waitcnt lgkmcnt(0)

; #define LAS __attribute__((address_space(3)))
; __device__ __forceinline__ void t128_load(const float* W, int N, int item, int lane, f32x4 (&v)[16]) {
;     const int nblk = N / 32, kb = item / nblk, nb = item % nblk, k0 = 128 * kb, n0 = 32 * nb;
; #pragma unroll
;     for (int i = 0; i < 16; ++i) v[i] = __builtin_nontemporal_load((const f32x4*)(W + (size_t)(k0 + i * 8 + (lane >> 3)) * N + n0 + (lane & 7) * 4));
; }
; template <int MODE>
; __device__ __forceinline__ void t128_store(const Ctx& c, const f32x4 (&v)[16], int K, int N, unsigned char* WT, int item) {
;     LAS float* scr = (LAS float*)(c.lds + c.wave * CONV_SCR);
;     const int nblk = N / 32, kb = item / nblk, nb = item % nblk, k0 = 128 * kb, n0 = 32 * nb, lane = c.lane;
; #pragma unroll
;     for (int i = 0; i < 16; ++i) { LAS float* d = scr + (i * 8 + (lane >> 3)) * 33 + (lane & 7) * 4; d[0] = v[i].x; d[1] = v[i].y; d[2] = v[i].z; d[3] = v[i].w; }
.Lcv7c_load:
	global_load_dwordx4 v[70:73], v[74:75], off nt
	global_load_dwordx4 v[66:69], v[76:77], off nt
	v_add_u32_e32 v74, 16, v122
	v_ashrrev_i32_e32 v75, 31, v74
	v_lshlrev_b64 v[74:75], s14, v[74:75]
	v_lshl_add_u64 v[82:83], v[124:125], 0, v[74:75]
	v_add_u32_e32 v74, 24, v122
	v_ashrrev_i32_e32 v75, 31, v74
	v_lshlrev_b64 v[74:75], s14, v[74:75]
	v_lshl_add_u64 v[84:85], v[124:125], 0, v[74:75]
	global_load_dwordx4 v[78:81], v[82:83], off nt
	global_load_dwordx4 v[74:77], v[84:85], off nt
	v_add_u32_e32 v82, 32, v122
	v_ashrrev_i32_e32 v83, 31, v82
	v_lshlrev_b64 v[82:83], s14, v[82:83]
	v_lshl_add_u64 v[90:91], v[124:125], 0, v[82:83]
	v_add_u32_e32 v82, 40, v122
	v_ashrrev_i32_e32 v83, 31, v82
	v_lshlrev_b64 v[82:83], s14, v[82:83]
	v_lshl_add_u64 v[92:93], v[124:125], 0, v[82:83]
	global_load_dwordx4 v[86:89], v[90:91], off nt
	global_load_dwordx4 v[82:85], v[92:93], off nt
	v_add_u32_e32 v90, 48, v122
	v_ashrrev_i32_e32 v91, 31, v90
	v_lshlrev_b64 v[90:91], s14, v[90:91]
	v_lshl_add_u64 v[98:99], v[124:125], 0, v[90:91]
	v_add_u32_e32 v90, 56, v122
	v_ashrrev_i32_e32 v91, 31, v90
	v_lshlrev_b64 v[90:91], s14, v[90:91]
	v_lshl_add_u64 v[100:101], v[124:125], 0, v[90:91]
	global_load_dwordx4 v[94:97], v[98:99], off nt
	global_load_dwordx4 v[90:93], v[100:101], off nt
	v_add_u32_e32 v98, 64, v122
	v_ashrrev_i32_e32 v99, 31, v98
	v_lshlrev_b64 v[98:99], s14, v[98:99]
	v_lshl_add_u64 v[106:107], v[124:125], 0, v[98:99]
	v_add_u32_e32 v98, 0x48, v122
	v_ashrrev_i32_e32 v99, 31, v98
	v_lshlrev_b64 v[98:99], s14, v[98:99]
	v_lshl_add_u64 v[108:109], v[124:125], 0, v[98:99]
	global_load_dwordx4 v[102:105], v[106:107], off nt
	global_load_dwordx4 v[98:101], v[108:109], off nt
	v_add_u32_e32 v106, 0x50, v122
	v_add_u32_e32 v108, 0x58, v122
	v_add_u32_e32 v114, 0x60, v122
	v_add_u32_e32 v116, 0x68, v122
	v_add_u32_e32 v126, 0x70, v122
	v_add_u32_e32 v122, 0x78, v122
	v_ashrrev_i32_e32 v107, 31, v106
	v_ashrrev_i32_e32 v109, 31, v108
	v_ashrrev_i32_e32 v115, 31, v114
	v_ashrrev_i32_e32 v117, 31, v116
	v_ashrrev_i32_e32 v127, 31, v126
	v_ashrrev_i32_e32 v123, 31, v122
	v_lshlrev_b64 v[106:107], s14, v[106:107]
	v_lshlrev_b64 v[108:109], s14, v[108:109]
	v_lshlrev_b64 v[114:115], s14, v[114:115]
	v_lshlrev_b64 v[116:117], s14, v[116:117]
	v_lshlrev_b64 v[126:127], s14, v[126:127]
	v_lshlrev_b64 v[122:123], s14, v[122:123]
	v_lshl_add_u64 v[106:107], v[124:125], 0, v[106:107]
	v_lshl_add_u64 v[108:109], v[124:125], 0, v[108:109]
	v_lshl_add_u64 v[114:115], v[124:125], 0, v[114:115]
	v_lshl_add_u64 v[116:117], v[124:125], 0, v[116:117]
	v_lshl_add_u64 v[126:127], v[124:125], 0, v[126:127]
	v_lshl_add_u64 v[122:123], v[124:125], 0, v[122:123]
	global_load_dwordx4 v[110:113], v[106:107], off nt
	s_nop 0
	global_load_dwordx4 v[106:109], v[108:109], off nt
	s_nop 0
	global_load_dwordx4 v[118:121], v[114:115], off nt
	s_nop 0
	global_load_dwordx4 v[114:117], v[116:117], off nt
	s_nop 0
	global_load_dwordx4 v[126:129], v[126:127], off nt
	s_nop 0
	global_load_dwordx4 v[122:125], v[122:123], off nt
.Lcv7c_noload:
	s_mov_b64 s[14:15], -1
	s_cmpk_gt_i32 s24, 0x7fff
	v_add_u32_e32 v145, 0x1080, v136
	v_add_u32_e32 v146, 0x1088, v136
	v_add_u32_e32 v147, 0x14a0, v136
	v_add_u32_e32 v148, 0x14a8, v136
	v_add_u32_e32 v149, 0x18c0, v136
	v_add_u32_e32 v150, 0x18c8, v136
	v_add_u32_e32 v151, 0x1ce0, v136
	v_add_u32_e32 v152, 0x1ce8, v136
	v_add_u32_e32 v153, 0x2100, v136
	v_add_u32_e32 v154, 0x2108, v136
	v_add_u32_e32 v155, 0x2520, v136
	v_add_u32_e32 v156, 0x2528, v136
	v_add_u32_e32 v157, 0x2940, v136
	v_add_u32_e32 v158, 0x2948, v136
	v_add_u32_e32 v159, 0x2d60, v136
	v_add_u32_e32 v160, 0x2d68, v136
	v_add_u32_e32 v161, 0x3180, v136
	v_add_u32_e32 v162, 0x3188, v136
	v_add_u32_e32 v163, 0x35a0, v136
	v_add_u32_e32 v164, 0x35a8, v136
	v_add_u32_e32 v165, 0x39c0, v136
	v_add_u32_e32 v166, 0x39c8, v136
	v_add_u32_e32 v167, 0x3de0, v136
	v_add_u32_e32 v168, 0x3de8, v136
	v_add_u32_e32 v144, 0x400, v1
	v_add_u32_e32 v143, 0x600, v1
	s_cbranch_scc0 .LBB0_1346
	s_waitcnt vmcnt(31)
	ds_write2_b32 v136, v6, v7 offset1:1
	ds_write2_b32 v136, v8, v9 offset0:2 offset1:3
	s_waitcnt vmcnt(30)
	ds_write2_b32 v140, v2, v3 offset1:1
	ds_write2_b32 v140, v4, v5 offset0:2 offset1:3
	s_waitcnt vmcnt(29)
	ds_write2_b32 v141, v14, v15 offset1:1
	ds_write2_b32 v141, v16, v17 offset0:2 offset1:3
	s_waitcnt vmcnt(28)
	ds_write2_b32 v142, v10, v11 offset1:1
	ds_write2_b32 v142, v12, v13 offset0:2 offset1:3
	s_waitcnt vmcnt(27)
	ds_write2_b32 v145, v22, v23 offset1:1
	ds_write2_b32 v146, v24, v25 offset1:1
	s_waitcnt vmcnt(26)
	ds_write2_b32 v147, v18, v19 offset1:1
	ds_write2_b32 v148, v20, v21 offset1:1
	s_waitcnt vmcnt(25)
	ds_write2_b32 v149, v30, v31 offset1:1
	ds_write2_b32 v150, v32, v33 offset1:1
	s_waitcnt vmcnt(24)
	ds_write2_b32 v151, v26, v27 offset1:1
	ds_write2_b32 v152, v28, v29 offset1:1
	s_waitcnt vmcnt(23)
	ds_write2_b32 v153, v38, v39 offset1:1
	ds_write2_b32 v154, v40, v41 offset1:1
	s_waitcnt vmcnt(22)
	ds_write2_b32 v155, v34, v35 offset1:1
	ds_write2_b32 v156, v36, v37 offset1:1
	s_waitcnt vmcnt(21)
	ds_write2_b32 v157, v46, v47 offset1:1
	ds_write2_b32 v158, v48, v49 offset1:1
	s_waitcnt vmcnt(20)
	ds_write2_b32 v159, v42, v43 offset1:1
	ds_write2_b32 v160, v44, v45 offset1:1
	s_waitcnt vmcnt(19)
	ds_write2_b32 v161, v54, v55 offset1:1
	ds_write2_b32 v162, v56, v57 offset1:1
	s_waitcnt vmcnt(18)
	ds_write2_b32 v163, v50, v51 offset1:1
	ds_write2_b32 v164, v52, v53 offset1:1
	s_waitcnt vmcnt(17)
	ds_write2_b32 v165, v62, v63 offset1:1
	ds_write2_b32 v166, v64, v65 offset1:1
	s_waitcnt vmcnt(16)
	ds_write2_b32 v167, v58, v59 offset1:1
	ds_write2_b32 v168, v60, v61 offset1:1
	s_waitcnt lgkmcnt(0)
; #define LAS __attribute__((address_space(3)))
; template <int MODE> __device__ __forceinline__ int drow_of(int n) {
;     if (MODE == 1) { const int bj = n / 2048, c = n % 2048; return 256 * (c / 128) + 128 * bj + (c % 128); }
; template <int MODE>
; __device__ __forceinline__ void t128_store(const Ctx& c, const f32x4 (&v)[16], int K, int N, unsigned char* WT, int item) {
;     ...
;     const int cc = lane & 7;
; #pragma unroll
;     for (int j = 0; j < 4; ++j) { const int n = (lane >> 3) + 8 * j; const LAS float* s = scr + (16 * cc) * 33 + n; int w[4];
; #pragma unroll
;         for (int q = 0; q < 4; ++q) { int t = 0; t = __builtin_amdgcn_cvt_pk_fp8_f32(s[(4 * q) * 33] * WSCALE, s[(4 * q + 1) * 33] * WSCALE, t, false);
;             t = __builtin_amdgcn_cvt_pk_fp8_f32(s[(4 * q + 2) * 33] * WSCALE, s[(4 * q + 3) * 33] * WSCALE, t, true); w[q] = t; }
;         const int dr = drow_of<MODE>(n0 + n);
;         __builtin_nontemporal_store((u32x4){(unsigned)w[0], (unsigned)w[1], (unsigned)w[2], (unsigned)w[3]}, (u32x4*)(WT + (size_t)dr * K + k0 + 16 * cc)); }
	ds_read2_b32 v[174:175], v1 offset1:8
	ds_read2_b32 v[176:177], v1 offset0:33 offset1:41
	ds_read2_b32 v[180:181], v1 offset0:66 offset1:74
	ds_read2_b32 v[182:183], v1 offset0:99 offset1:107
	v_mov_b32_e32 v170, v133
	ds_read2_b32 v[184:185], v1 offset0:132 offset1:140
	ds_read2_b32 v[186:187], v1 offset0:165 offset1:173
	s_waitcnt lgkmcnt(5)
	v_mul_f32_e32 v169, 0x42800000, v174
	s_waitcnt lgkmcnt(4)
	v_mul_f32_e32 v171, 0x42800000, v176
	v_cvt_pk_fp8_f32 v170, v169, v171
	s_waitcnt lgkmcnt(3)
	v_mul_f32_e32 v169, 0x42800000, v180
	s_waitcnt lgkmcnt(2)
	v_mul_f32_e32 v171, 0x42800000, v182
	ds_read2_b32 v[188:189], v1 offset0:198 offset1:206
	ds_read2_b32 v[190:191], v1 offset0:231 offset1:239
	v_cvt_pk_fp8_f32 v170, v169, v171 op_sel:[0,0,1]
	s_waitcnt lgkmcnt(3)
	v_mul_f32_e32 v169, 0x42800000, v184
	s_waitcnt lgkmcnt(2)
	v_mul_f32_e32 v172, 0x42800000, v186
	v_mov_b32_e32 v171, v133
	ds_read2_b32 v[192:193], v144 offset0:8 offset1:16
	ds_read2_b32 v[194:195], v144 offset0:41 offset1:49
	v_cvt_pk_fp8_f32 v171, v169, v172
	ds_read2_b32 v[196:197], v144 offset0:74 offset1:82
	ds_read2_b32 v[198:199], v144 offset0:107 offset1:115
	ds_read2_b32 v[200:201], v144 offset0:140 offset1:148
	ds_read2_b32 v[202:203], v144 offset0:173 offset1:181
	s_add_i32 s8, s24, 0xffff8000
	s_lshr_b32 s8, s8, 11
	s_waitcnt lgkmcnt(7)
	v_mul_f32_e32 v169, 0x42800000, v188
	s_waitcnt lgkmcnt(6)
	v_mul_f32_e32 v172, 0x42800000, v190
	s_lshl_b64 s[14:15], s[8:9], 23
	v_cvt_pk_fp8_f32 v171, v169, v172 op_sel:[0,0,1]
	s_waitcnt lgkmcnt(5)
	v_mul_f32_e32 v169, 0x42800000, v192
	s_waitcnt lgkmcnt(4)
	v_mul_f32_e32 v173, 0x42800000, v194
	v_mov_b32_e32 v172, v133
	ds_read2_b32 v[204:205], v144 offset0:206 offset1:214
	ds_read2_b32 v[206:207], v144 offset0:239 offset1:247
	s_add_u32 s8, s52, s14
	v_cvt_pk_fp8_f32 v172, v169, v173
	s_waitcnt lgkmcnt(3)
	v_mul_f32_e32 v176, 0x42800000, v200
	s_waitcnt lgkmcnt(2)
	v_mul_f32_e32 v180, 0x42800000, v202
	v_mov_b32_e32 v173, v133
	s_addc_u32 s15, s53, s15
	s_lshl_b32 s16, s24, 5
	s_and_b32 s14, s24, 0x780
	v_cvt_pk_fp8_f32 v173, v176, v180
	s_add_u32 s14, s8, s14
	s_addc_u32 s15, s15, 0
	v_mul_f32_e32 v169, 0x42800000, v196
	v_mul_f32_e32 v174, 0x42800000, v198
	s_lshl_b32 s8, s24, 6
	v_lshl_add_u64 v[178:179], s[14:15], 0, v[134:135]
	v_cvt_pk_fp8_f32 v172, v169, v174 op_sel:[0,0,1]
	s_waitcnt lgkmcnt(1)
	v_mul_f32_e32 v169, 0x42800000, v204
	s_waitcnt lgkmcnt(0)
	v_mul_f32_e32 v174, 0x42800000, v206
	s_and_b32 s8, s8, 0xf00
	s_lshl_b32 s14, s24, 1
	s_and_b32 s15, s16, 0x60
	v_cvt_pk_fp8_f32 v173, v169, v174 op_sel:[0,0,1]
	s_and_b32 s14, s14, 0x80
	s_or_b32 s8, s15, s8
	s_or_b32 s8, s8, s14
	v_add_lshl_u32 v208, s8, v131, 11
	v_mov_b32_e32 v209, v133
	v_lshl_add_u64 v[208:209], v[178:179], 0, v[208:209]
	global_store_dwordx4 v[208:209], v[170:173], off nt
	v_mul_f32_e32 v169, 0x42800000, v175
	v_mul_f32_e32 v174, 0x42800000, v187
	v_mul_f32_e32 v171, 0x42800000, v177
	v_mov_b32_e32 v170, v133
	v_cvt_pk_fp8_f32 v170, v169, v171
	v_mul_f32_e32 v173, 0x42800000, v185
	v_mov_b32_e32 v171, v133
	v_cvt_pk_fp8_f32 v171, v173, v174
	v_mul_f32_e32 v169, 0x42800000, v181
	v_mul_f32_e32 v172, 0x42800000, v183
	v_cvt_pk_fp8_f32 v170, v169, v172 op_sel:[0,0,1]
	v_mul_f32_e32 v169, 0x42800000, v189
	v_mul_f32_e32 v172, 0x42800000, v191
	v_cvt_pk_fp8_f32 v171, v169, v172 op_sel:[0,0,1]
	v_mul_f32_e32 v169, 0x42800000, v193
	v_mul_f32_e32 v173, 0x42800000, v195
	v_mov_b32_e32 v172, v133
	v_cvt_pk_fp8_f32 v172, v169, v173
	v_mul_f32_e32 v175, 0x42800000, v201
	v_mul_f32_e32 v176, 0x42800000, v203
	v_mov_b32_e32 v173, v133
	v_cvt_pk_fp8_f32 v173, v175, v176
	v_mul_f32_e32 v169, 0x42800000, v197
	v_mul_f32_e32 v174, 0x42800000, v199
	v_cvt_pk_fp8_f32 v172, v169, v174 op_sel:[0,0,1]
	v_mul_f32_e32 v169, 0x42800000, v205
	v_mul_f32_e32 v174, 0x42800000, v207
	v_cvt_pk_fp8_f32 v173, v169, v174 op_sel:[0,0,1]
	ds_read2_b32 v[176:177], v1 offset0:16 offset1:24
	ds_read2_b32 v[180:181], v1 offset0:49 offset1:57
	v_add_lshl_u32 v174, s8, v137, 11
	v_mov_b32_e32 v175, v133
	v_lshl_add_u64 v[174:175], v[178:179], 0, v[174:175]
	global_store_dwordx4 v[174:175], v[170:173], off nt
	ds_read2_b32 v[174:175], v1 offset0:82 offset1:90
	ds_read2_b32 v[182:183], v1 offset0:115 offset1:123
	s_waitcnt lgkmcnt(3)
; #define LAS __attribute__((address_space(3)))
; #define LDS_WAIT() asm volatile("s_waitcnt lgkmcnt(0)" ::: "memory")
; template <int MODE>
; __device__ __forceinline__ void t128_store(const Ctx& c, const f32x4 (&v)[16], int K, int N, unsigned char* WT, int item) {
;     ...
;     const int cc = lane & 7;
; #pragma unroll
;     for (int j = 0; j < 4; ++j) { const int n = (lane >> 3) + 8 * j; const LAS float* s = scr + (16 * cc) * 33 + n; int w[4];
; #pragma unroll
;         for (int q = 0; q < 4; ++q) { int t = 0; t = __builtin_amdgcn_cvt_pk_fp8_f32(s[(4 * q) * 33] * WSCALE, s[(4 * q + 1) * 33] * WSCALE, t, false);
;             t = __builtin_amdgcn_cvt_pk_fp8_f32(s[(4 * q + 2) * 33] * WSCALE, s[(4 * q + 3) * 33] * WSCALE, t, true); w[q] = t; }
;         const int dr = drow_of<MODE>(n0 + n);
;         __builtin_nontemporal_store((u32x4){(unsigned)w[0], (unsigned)w[1], (unsigned)w[2], (unsigned)w[3]}, (u32x4*)(WT + (size_t)dr * K + k0 + 16 * cc)); }
;     LDS_WAIT(); asm volatile("" ::: "memory");
	v_mul_f32_e32 v169, 0x42800000, v176
	s_waitcnt lgkmcnt(2)
	v_mul_f32_e32 v171, 0x42800000, v180
	v_mov_b32_e32 v170, v133
	ds_read2_b32 v[184:185], v1 offset0:148 offset1:156
	ds_read2_b32 v[186:187], v1 offset0:181 offset1:189
	v_cvt_pk_fp8_f32 v170, v169, v171
	s_waitcnt lgkmcnt(3)
	v_mul_f32_e32 v169, 0x42800000, v174
	s_waitcnt lgkmcnt(2)
	v_mul_f32_e32 v171, 0x42800000, v182
	ds_read2_b32 v[188:189], v1 offset0:214 offset1:222
	ds_read2_b32 v[190:191], v1 offset0:247 offset1:255
	v_cvt_pk_fp8_f32 v170, v169, v171 op_sel:[0,0,1]
	s_waitcnt lgkmcnt(3)
	v_mul_f32_e32 v169, 0x42800000, v184
	s_waitcnt lgkmcnt(2)
	v_mul_f32_e32 v172, 0x42800000, v186
	v_mov_b32_e32 v171, v133
	ds_read2_b32 v[192:193], v144 offset0:24 offset1:32
	ds_read2_b32 v[194:195], v144 offset0:57 offset1:65
	v_cvt_pk_fp8_f32 v171, v169, v172
	ds_read2_b32 v[196:197], v144 offset0:90 offset1:98
	ds_read2_b32 v[198:199], v144 offset0:123 offset1:131
	ds_read2_b32 v[200:201], v144 offset0:156 offset1:164
	ds_read2_b32 v[202:203], v144 offset0:189 offset1:197
	s_waitcnt lgkmcnt(7)
	v_mul_f32_e32 v169, 0x42800000, v188
	s_waitcnt lgkmcnt(6)
	v_mul_f32_e32 v172, 0x42800000, v190
	v_cvt_pk_fp8_f32 v171, v169, v172 op_sel:[0,0,1]
	s_waitcnt lgkmcnt(5)
	v_mul_f32_e32 v169, 0x42800000, v192
	s_waitcnt lgkmcnt(4)
	v_mul_f32_e32 v173, 0x42800000, v194
	v_mov_b32_e32 v172, v133
	ds_read2_b32 v[204:205], v144 offset0:222 offset1:230
	ds_read2_b32 v[206:207], v143 offset0:127 offset1:135
	v_cvt_pk_fp8_f32 v172, v169, v173
	s_waitcnt lgkmcnt(3)
	v_mul_f32_e32 v176, 0x42800000, v200
	s_waitcnt lgkmcnt(2)
	v_mul_f32_e32 v180, 0x42800000, v202
	v_mov_b32_e32 v173, v133
	v_cvt_pk_fp8_f32 v173, v176, v180
	v_mul_f32_e32 v169, 0x42800000, v196
	v_mul_f32_e32 v174, 0x42800000, v198
	v_cvt_pk_fp8_f32 v172, v169, v174 op_sel:[0,0,1]
	s_waitcnt lgkmcnt(1)
	v_mul_f32_e32 v169, 0x42800000, v204
	s_waitcnt lgkmcnt(0)
	v_mul_f32_e32 v174, 0x42800000, v206
	v_cvt_pk_fp8_f32 v173, v169, v174 op_sel:[0,0,1]
	v_add_lshl_u32 v208, s8, v138, 11
	v_mov_b32_e32 v209, v133
	v_lshl_add_u64 v[208:209], v[178:179], 0, v[208:209]
	global_store_dwordx4 v[208:209], v[170:173], off nt
	v_mul_f32_e32 v169, 0x42800000, v177
	v_mul_f32_e32 v174, 0x42800000, v187
	v_mul_f32_e32 v171, 0x42800000, v181
	v_mov_b32_e32 v170, v133
	v_cvt_pk_fp8_f32 v170, v169, v171
	v_mul_f32_e32 v173, 0x42800000, v185
	v_mov_b32_e32 v171, v133
	v_cvt_pk_fp8_f32 v171, v173, v174
	v_mul_f32_e32 v169, 0x42800000, v175
	v_mul_f32_e32 v172, 0x42800000, v183
	v_cvt_pk_fp8_f32 v170, v169, v172 op_sel:[0,0,1]
	v_mul_f32_e32 v169, 0x42800000, v189
	v_mul_f32_e32 v172, 0x42800000, v191
	v_cvt_pk_fp8_f32 v171, v169, v172 op_sel:[0,0,1]
	v_mul_f32_e32 v169, 0x42800000, v193
	v_mul_f32_e32 v173, 0x42800000, v195
	v_mov_b32_e32 v172, v133
	v_cvt_pk_fp8_f32 v172, v169, v173
	v_mul_f32_e32 v175, 0x42800000, v201
	v_mul_f32_e32 v176, 0x42800000, v203
	v_mov_b32_e32 v173, v133
	v_cvt_pk_fp8_f32 v173, v175, v176
	v_mul_f32_e32 v169, 0x42800000, v197
	v_mul_f32_e32 v174, 0x42800000, v199
	v_cvt_pk_fp8_f32 v172, v169, v174 op_sel:[0,0,1]
	v_mul_f32_e32 v169, 0x42800000, v205
	v_mul_f32_e32 v174, 0x42800000, v207
	v_cvt_pk_fp8_f32 v173, v169, v174 op_sel:[0,0,1]
	v_add_lshl_u32 v174, s8, v139, 11
	v_mov_b32_e32 v175, v133
	v_lshl_add_u64 v[174:175], v[178:179], 0, v[174:175]
	global_store_dwordx4 v[174:175], v[170:173], off nt
	s_waitcnt lgkmcnt(0)
	s_cbranch_execnz .LBB0_1348
	s_branch .LBB0_1347

; #define LAS __attribute__((address_space(3)))
; __device__ __forceinline__ void t128_load(const float* W, int N, int item, int lane, f32x4 (&v)[16]) {
;     const int nblk = N / 32, kb = item / nblk, nb = item % nblk, k0 = 128 * kb, n0 = 32 * nb;
; #pragma unroll
;     for (int i = 0; i < 16; ++i) v[i] = __builtin_nontemporal_load((const f32x4*)(W + (size_t)(k0 + i * 8 + (lane >> 3)) * N + n0 + (lane & 7) * 4));
; }
; template <int MODE>
; __device__ __forceinline__ void t128_store(const Ctx& c, const f32x4 (&v)[16], int K, int N, unsigned char* WT, int item) {
;     LAS float* scr = (LAS float*)(c.lds + c.wave * CONV_SCR);
;     const int nblk = N / 32, kb = item / nblk, nb = item % nblk, k0 = 128 * kb, n0 = 32 * nb, lane = c.lane;
; #pragma unroll
;     for (int i = 0; i < 16; ++i) { LAS float* d = scr + (i * 8 + (lane >> 3)) * 33 + (lane & 7) * 4; d[0] = v[i].x; d[1] = v[i].y; d[2] = v[i].z; d[3] = v[i].w; }
.Lcv7d_load:
	global_load_dwordx4 v[6:9], v[10:11], off nt
	global_load_dwordx4 v[2:5], v[12:13], off nt
	v_add_u32_e32 v10, 16, v58
	v_ashrrev_i32_e32 v11, 31, v10
	v_lshlrev_b64 v[10:11], s14, v[10:11]
	v_lshl_add_u64 v[18:19], v[60:61], 0, v[10:11]
	v_add_u32_e32 v10, 24, v58
	v_ashrrev_i32_e32 v11, 31, v10
	v_lshlrev_b64 v[10:11], s14, v[10:11]
	v_lshl_add_u64 v[20:21], v[60:61], 0, v[10:11]
	global_load_dwordx4 v[14:17], v[18:19], off nt
	global_load_dwordx4 v[10:13], v[20:21], off nt
	v_add_u32_e32 v18, 32, v58
	v_add_u32_e32 v20, 40, v58
	v_add_u32_e32 v26, 48, v58
	v_add_u32_e32 v28, 56, v58
	v_add_u32_e32 v34, 64, v58
	v_add_u32_e32 v36, 0x48, v58
	v_add_u32_e32 v42, 0x50, v58
	v_add_u32_e32 v44, 0x58, v58
	v_add_u32_e32 v50, 0x60, v58
	v_add_u32_e32 v52, 0x68, v58
	v_add_u32_e32 v62, 0x70, v58
	v_add_u32_e32 v58, 0x78, v58
	v_ashrrev_i32_e32 v19, 31, v18
	v_ashrrev_i32_e32 v21, 31, v20
	v_ashrrev_i32_e32 v27, 31, v26
	v_ashrrev_i32_e32 v29, 31, v28
	v_ashrrev_i32_e32 v35, 31, v34
	v_ashrrev_i32_e32 v37, 31, v36
	v_ashrrev_i32_e32 v43, 31, v42
	v_ashrrev_i32_e32 v45, 31, v44
	v_ashrrev_i32_e32 v51, 31, v50
	v_ashrrev_i32_e32 v53, 31, v52
	v_ashrrev_i32_e32 v63, 31, v62
	v_ashrrev_i32_e32 v59, 31, v58
	v_lshlrev_b64 v[18:19], s14, v[18:19]
	v_lshlrev_b64 v[20:21], s14, v[20:21]
	v_lshlrev_b64 v[26:27], s14, v[26:27]
	v_lshlrev_b64 v[28:29], s14, v[28:29]
	v_lshlrev_b64 v[34:35], s14, v[34:35]
	v_lshlrev_b64 v[36:37], s14, v[36:37]
	v_lshlrev_b64 v[42:43], s14, v[42:43]
	v_lshlrev_b64 v[44:45], s14, v[44:45]
	v_lshlrev_b64 v[50:51], s14, v[50:51]
	v_lshlrev_b64 v[52:53], s14, v[52:53]
	v_lshlrev_b64 v[62:63], s14, v[62:63]
	v_lshlrev_b64 v[58:59], s14, v[58:59]
	v_lshl_add_u64 v[18:19], v[60:61], 0, v[18:19]
	v_lshl_add_u64 v[20:21], v[60:61], 0, v[20:21]
	v_lshl_add_u64 v[26:27], v[60:61], 0, v[26:27]
	v_lshl_add_u64 v[28:29], v[60:61], 0, v[28:29]
	v_lshl_add_u64 v[34:35], v[60:61], 0, v[34:35]
	v_lshl_add_u64 v[36:37], v[60:61], 0, v[36:37]
	v_lshl_add_u64 v[42:43], v[60:61], 0, v[42:43]
	v_lshl_add_u64 v[44:45], v[60:61], 0, v[44:45]
	v_lshl_add_u64 v[50:51], v[60:61], 0, v[50:51]
	v_lshl_add_u64 v[52:53], v[60:61], 0, v[52:53]
	v_lshl_add_u64 v[62:63], v[60:61], 0, v[62:63]
	v_lshl_add_u64 v[58:59], v[60:61], 0, v[58:59]
	global_load_dwordx4 v[22:25], v[18:19], off nt
	s_nop 0
	global_load_dwordx4 v[18:21], v[20:21], off nt
	s_nop 0
	global_load_dwordx4 v[30:33], v[26:27], off nt
	s_nop 0
	global_load_dwordx4 v[26:29], v[28:29], off nt
	s_nop 0
	global_load_dwordx4 v[38:41], v[34:35], off nt
	s_nop 0
	global_load_dwordx4 v[34:37], v[36:37], off nt
	s_nop 0
	global_load_dwordx4 v[46:49], v[42:43], off nt
	s_nop 0
	global_load_dwordx4 v[42:45], v[44:45], off nt
	s_nop 0
	global_load_dwordx4 v[54:57], v[50:51], off nt
	s_nop 0
	global_load_dwordx4 v[50:53], v[52:53], off nt
	s_nop 0
	global_load_dwordx4 v[62:65], v[62:63], off nt
	s_nop 0
	global_load_dwordx4 v[58:61], v[58:59], off nt
.Lcv7d_noload:
	s_mov_b64 s[14:15], -1
	s_and_b64 vcc, exec, s[10:11]
	s_cbranch_vccz .LBB0_1360
	s_waitcnt vmcnt(31)
	ds_write2_b32 v136, v70, v71 offset1:1
	ds_write2_b32 v136, v72, v73 offset0:2 offset1:3
	s_waitcnt vmcnt(30)
	ds_write2_b32 v140, v66, v67 offset1:1
	ds_write2_b32 v140, v68, v69 offset0:2 offset1:3
	s_waitcnt vmcnt(29)
	ds_write2_b32 v141, v78, v79 offset1:1
	ds_write2_b32 v141, v80, v81 offset0:2 offset1:3
	s_waitcnt vmcnt(28)
	ds_write2_b32 v142, v74, v75 offset1:1
	ds_write2_b32 v142, v76, v77 offset0:2 offset1:3
	s_waitcnt vmcnt(27)
	ds_write2_b32 v145, v86, v87 offset1:1
	ds_write2_b32 v146, v88, v89 offset1:1
	s_waitcnt vmcnt(26)
	ds_write2_b32 v147, v82, v83 offset1:1
	ds_write2_b32 v148, v84, v85 offset1:1
	s_waitcnt vmcnt(25)
	ds_write2_b32 v149, v94, v95 offset1:1
	ds_write2_b32 v150, v96, v97 offset1:1
	s_waitcnt vmcnt(24)
	ds_write2_b32 v151, v90, v91 offset1:1
	ds_write2_b32 v152, v92, v93 offset1:1
	s_waitcnt vmcnt(23)
	ds_write2_b32 v153, v102, v103 offset1:1
	ds_write2_b32 v154, v104, v105 offset1:1
	s_waitcnt vmcnt(22)
	ds_write2_b32 v155, v98, v99 offset1:1
	ds_write2_b32 v156, v100, v101 offset1:1
	s_waitcnt vmcnt(21)
	ds_write2_b32 v157, v110, v111 offset1:1
	ds_write2_b32 v158, v112, v113 offset1:1
	s_waitcnt vmcnt(20)
	ds_write2_b32 v159, v106, v107 offset1:1
	ds_write2_b32 v160, v108, v109 offset1:1
	s_waitcnt vmcnt(19)
	ds_write2_b32 v161, v118, v119 offset1:1
	ds_write2_b32 v162, v120, v121 offset1:1
	s_waitcnt vmcnt(18)
	ds_write2_b32 v163, v114, v115 offset1:1
	ds_write2_b32 v164, v116, v117 offset1:1
	s_waitcnt vmcnt(17)
	ds_write2_b32 v165, v126, v127 offset1:1
	ds_write2_b32 v166, v128, v129 offset1:1
	s_waitcnt vmcnt(16)
	ds_write2_b32 v167, v122, v123 offset1:1
	ds_write2_b32 v168, v124, v125 offset1:1
	s_waitcnt lgkmcnt(0)
	ds_read2_b32 v[174:175], v1 offset1:8
	ds_read2_b32 v[176:177], v1 offset0:33 offset1:41
	ds_read2_b32 v[180:181], v1 offset0:66 offset1:74
	ds_read2_b32 v[182:183], v1 offset0:99 offset1:107
	v_mov_b32_e32 v170, v133
	ds_read2_b32 v[184:185], v1 offset0:132 offset1:140
	ds_read2_b32 v[186:187], v1 offset0:165 offset1:173
	s_waitcnt lgkmcnt(5)
	v_mul_f32_e32 v132, 0x42800000, v174
	s_waitcnt lgkmcnt(4)
	v_mul_f32_e32 v169, 0x42800000, v176
	v_cvt_pk_fp8_f32 v170, v132, v169
	s_waitcnt lgkmcnt(3)
	v_mul_f32_e32 v132, 0x42800000, v180
	s_waitcnt lgkmcnt(2)
	v_mul_f32_e32 v169, 0x42800000, v182
	ds_read2_b32 v[188:189], v1 offset0:198 offset1:206
	ds_read2_b32 v[190:191], v1 offset0:231 offset1:239
	v_cvt_pk_fp8_f32 v170, v132, v169 op_sel:[0,0,1]
	s_waitcnt lgkmcnt(3)
	v_mul_f32_e32 v132, 0x42800000, v184
	s_waitcnt lgkmcnt(2)
; #define LAS __attribute__((address_space(3)))
; #define LDS_WAIT() asm volatile("s_waitcnt lgkmcnt(0)" ::: "memory")
; template <int MODE>
; __device__ __forceinline__ void t128_store(const Ctx& c, const f32x4 (&v)[16], int K, int N, unsigned char* WT, int item) {
;     ...
;     const int cc = lane & 7;
; #pragma unroll
;     for (int j = 0; j < 4; ++j) { const int n = (lane >> 3) + 8 * j; const LAS float* s = scr + (16 * cc) * 33 + n; int w[4];
; #pragma unroll
;         for (int q = 0; q < 4; ++q) { int t = 0; t = __builtin_amdgcn_cvt_pk_fp8_f32(s[(4 * q) * 33] * WSCALE, s[(4 * q + 1) * 33] * WSCALE, t, false);
;             t = __builtin_amdgcn_cvt_pk_fp8_f32(s[(4 * q + 2) * 33] * WSCALE, s[(4 * q + 3) * 33] * WSCALE, t, true); w[q] = t; }
;         const int dr = drow_of<MODE>(n0 + n);
;         __builtin_nontemporal_store((u32x4){(unsigned)w[0], (unsigned)w[1], (unsigned)w[2], (unsigned)w[3]}, (u32x4*)(WT + (size_t)dr * K + k0 + 16 * cc)); }
;     LDS_WAIT(); asm volatile("" ::: "memory");
	v_mul_f32_e32 v169, 0x42800000, v186
	v_mov_b32_e32 v171, v133
	ds_read2_b32 v[192:193], v144 offset0:8 offset1:16
	ds_read2_b32 v[194:195], v144 offset0:41 offset1:49
	v_cvt_pk_fp8_f32 v171, v132, v169
	ds_read2_b32 v[196:197], v144 offset0:74 offset1:82
	ds_read2_b32 v[198:199], v144 offset0:107 offset1:115
	ds_read2_b32 v[200:201], v144 offset0:140 offset1:148
	ds_read2_b32 v[202:203], v144 offset0:173 offset1:181
	s_add_i32 s8, s25, 0xffff8000
	s_lshr_b32 s8, s8, 11
	s_waitcnt lgkmcnt(7)
	v_mul_f32_e32 v132, 0x42800000, v188
	s_waitcnt lgkmcnt(6)
	v_mul_f32_e32 v169, 0x42800000, v190
	s_lshl_b64 s[10:11], s[8:9], 23
	v_cvt_pk_fp8_f32 v171, v132, v169 op_sel:[0,0,1]
	s_waitcnt lgkmcnt(5)
	v_mul_f32_e32 v132, 0x42800000, v192
	s_waitcnt lgkmcnt(4)
	v_mul_f32_e32 v169, 0x42800000, v194
	v_mov_b32_e32 v172, v133
	ds_read2_b32 v[204:205], v144 offset0:206 offset1:214
	ds_read2_b32 v[206:207], v144 offset0:239 offset1:247
	s_add_u32 s8, s52, s10
	v_cvt_pk_fp8_f32 v172, v132, v169
	s_waitcnt lgkmcnt(3)
	v_mul_f32_e32 v174, 0x42800000, v200
	s_waitcnt lgkmcnt(2)
	v_mul_f32_e32 v176, 0x42800000, v202
	v_mov_b32_e32 v173, v133
	s_addc_u32 s11, s53, s11
	s_lshl_b32 s14, s25, 5
	s_and_b32 s10, s25, 0x780
	v_cvt_pk_fp8_f32 v173, v174, v176
	s_add_u32 s10, s8, s10
	s_addc_u32 s11, s11, 0
	v_mul_f32_e32 v132, 0x42800000, v196
	v_mul_f32_e32 v169, 0x42800000, v198
	s_lshl_b32 s8, s25, 6
	v_lshl_add_u64 v[178:179], s[10:11], 0, v[134:135]
	v_cvt_pk_fp8_f32 v172, v132, v169 op_sel:[0,0,1]
	s_waitcnt lgkmcnt(1)
	v_mul_f32_e32 v132, 0x42800000, v204
	s_waitcnt lgkmcnt(0)
	v_mul_f32_e32 v169, 0x42800000, v206
	s_and_b32 s8, s8, 0xf00
	s_lshl_b32 s10, s25, 1
	s_and_b32 s11, s14, 0x60
	v_cvt_pk_fp8_f32 v173, v132, v169 op_sel:[0,0,1]
	s_and_b32 s10, s10, 0x80
	s_or_b32 s8, s11, s8
	s_or_b32 s8, s8, s10
	v_add_lshl_u32 v132, s8, v131, 11
	v_lshl_add_u64 v[208:209], v[178:179], 0, v[132:133]
	global_store_dwordx4 v[208:209], v[170:173], off nt
	v_mul_f32_e32 v132, 0x42800000, v175
	v_mul_f32_e32 v169, 0x42800000, v177
	v_mov_b32_e32 v170, v133
	v_cvt_pk_fp8_f32 v170, v132, v169
	v_mul_f32_e32 v172, 0x42800000, v185
	v_mul_f32_e32 v173, 0x42800000, v187
	v_mov_b32_e32 v171, v133
	v_cvt_pk_fp8_f32 v171, v172, v173
	v_mul_f32_e32 v132, 0x42800000, v181
	v_mul_f32_e32 v169, 0x42800000, v183
	v_cvt_pk_fp8_f32 v170, v132, v169 op_sel:[0,0,1]
	v_mul_f32_e32 v132, 0x42800000, v189
	v_mul_f32_e32 v169, 0x42800000, v191
	v_cvt_pk_fp8_f32 v171, v132, v169 op_sel:[0,0,1]
	v_mul_f32_e32 v132, 0x42800000, v193
	v_mul_f32_e32 v169, 0x42800000, v195
	v_mov_b32_e32 v172, v133
	v_cvt_pk_fp8_f32 v172, v132, v169
	v_mul_f32_e32 v174, 0x42800000, v201
	v_mul_f32_e32 v175, 0x42800000, v203
	v_mov_b32_e32 v173, v133
	v_cvt_pk_fp8_f32 v173, v174, v175
	v_mul_f32_e32 v132, 0x42800000, v197
	v_mul_f32_e32 v169, 0x42800000, v199
	v_cvt_pk_fp8_f32 v172, v132, v169 op_sel:[0,0,1]
	v_mul_f32_e32 v132, 0x42800000, v205
	v_mul_f32_e32 v169, 0x42800000, v207
	v_cvt_pk_fp8_f32 v173, v132, v169 op_sel:[0,0,1]
	ds_read2_b32 v[174:175], v1 offset0:16 offset1:24
	ds_read2_b32 v[176:177], v1 offset0:49 offset1:57
	v_add_lshl_u32 v132, s8, v137, 11
	v_lshl_add_u64 v[180:181], v[178:179], 0, v[132:133]
	global_store_dwordx4 v[180:181], v[170:173], off nt
	ds_read2_b32 v[180:181], v1 offset0:82 offset1:90
	ds_read2_b32 v[182:183], v1 offset0:115 offset1:123
	s_waitcnt lgkmcnt(3)
	v_mul_f32_e32 v132, 0x42800000, v174
	s_waitcnt lgkmcnt(2)
	v_mul_f32_e32 v169, 0x42800000, v176
	v_mov_b32_e32 v170, v133
	ds_read2_b32 v[184:185], v1 offset0:148 offset1:156
	ds_read2_b32 v[186:187], v1 offset0:181 offset1:189
	v_cvt_pk_fp8_f32 v170, v132, v169
	s_waitcnt lgkmcnt(3)
	v_mul_f32_e32 v132, 0x42800000, v180
	s_waitcnt lgkmcnt(2)
	v_mul_f32_e32 v169, 0x42800000, v182
	ds_read2_b32 v[188:189], v1 offset0:214 offset1:222
	ds_read2_b32 v[190:191], v1 offset0:247 offset1:255
	v_cvt_pk_fp8_f32 v170, v132, v169 op_sel:[0,0,1]
	s_waitcnt lgkmcnt(3)
	v_mul_f32_e32 v132, 0x42800000, v184
	s_waitcnt lgkmcnt(2)
	v_mul_f32_e32 v169, 0x42800000, v186
	v_mov_b32_e32 v171, v133
	ds_read2_b32 v[192:193], v144 offset0:24 offset1:32
	ds_read2_b32 v[194:195], v144 offset0:57 offset1:65
	v_cvt_pk_fp8_f32 v171, v132, v169
	ds_read2_b32 v[196:197], v144 offset0:90 offset1:98
	ds_read2_b32 v[198:199], v144 offset0:123 offset1:131
	ds_read2_b32 v[200:201], v144 offset0:156 offset1:164
	ds_read2_b32 v[202:203], v144 offset0:189 offset1:197
	s_waitcnt lgkmcnt(7)
	v_mul_f32_e32 v132, 0x42800000, v188
	s_waitcnt lgkmcnt(6)
	v_mul_f32_e32 v169, 0x42800000, v190
	v_cvt_pk_fp8_f32 v171, v132, v169 op_sel:[0,0,1]
	s_waitcnt lgkmcnt(5)
	v_mul_f32_e32 v132, 0x42800000, v192
	s_waitcnt lgkmcnt(4)
	v_mul_f32_e32 v169, 0x42800000, v194
	v_mov_b32_e32 v172, v133
	ds_read2_b32 v[204:205], v144 offset0:222 offset1:230
	ds_read2_b32 v[206:207], v143 offset0:127 offset1:135
	v_cvt_pk_fp8_f32 v172, v132, v169
	s_waitcnt lgkmcnt(3)
	v_mul_f32_e32 v174, 0x42800000, v200
	s_waitcnt lgkmcnt(2)
	v_mul_f32_e32 v176, 0x42800000, v202
	v_mov_b32_e32 v173, v133
	v_cvt_pk_fp8_f32 v173, v174, v176
	v_mul_f32_e32 v132, 0x42800000, v196
	v_mul_f32_e32 v169, 0x42800000, v198
	v_cvt_pk_fp8_f32 v172, v132, v169 op_sel:[0,0,1]
	s_waitcnt lgkmcnt(1)
	v_mul_f32_e32 v132, 0x42800000, v204
	s_waitcnt lgkmcnt(0)
	v_mul_f32_e32 v169, 0x42800000, v206
	v_cvt_pk_fp8_f32 v173, v132, v169 op_sel:[0,0,1]
	v_add_lshl_u32 v132, s8, v138, 11
	v_lshl_add_u64 v[208:209], v[178:179], 0, v[132:133]
	v_mul_f32_e32 v132, 0x42800000, v175
	v_mul_f32_e32 v169, 0x42800000, v177
	v_mov_b32_e32 v174, v133
	v_cvt_pk_fp8_f32 v174, v132, v169
	v_mul_f32_e32 v176, 0x42800000, v185
	v_mul_f32_e32 v177, 0x42800000, v187
	v_mov_b32_e32 v175, v133
	v_cvt_pk_fp8_f32 v175, v176, v177
	v_mul_f32_e32 v132, 0x42800000, v181
	v_mul_f32_e32 v169, 0x42800000, v183
	v_cvt_pk_fp8_f32 v174, v132, v169 op_sel:[0,0,1]
	v_mul_f32_e32 v132, 0x42800000, v189
	v_mul_f32_e32 v169, 0x42800000, v191
	v_cvt_pk_fp8_f32 v175, v132, v169 op_sel:[0,0,1]
	v_mul_f32_e32 v132, 0x42800000, v193
	v_mul_f32_e32 v169, 0x42800000, v195
	v_mov_b32_e32 v176, v133
	v_cvt_pk_fp8_f32 v176, v132, v169
	v_mul_f32_e32 v180, 0x42800000, v201
	v_mul_f32_e32 v181, 0x42800000, v203
	v_mov_b32_e32 v177, v133
	v_cvt_pk_fp8_f32 v177, v180, v181
	v_mul_f32_e32 v132, 0x42800000, v197
	v_mul_f32_e32 v169, 0x42800000, v199
	v_cvt_pk_fp8_f32 v176, v132, v169 op_sel:[0,0,1]
	v_mul_f32_e32 v132, 0x42800000, v205
	v_mul_f32_e32 v169, 0x42800000, v207
	v_cvt_pk_fp8_f32 v177, v132, v169 op_sel:[0,0,1]
	v_add_lshl_u32 v132, s8, v139, 11
	global_store_dwordx4 v[208:209], v[170:173], off nt
	s_mov_b64 s[14:15], 0
	s_nop 0
	v_lshl_add_u64 v[170:171], v[178:179], 0, v[132:133]
	global_store_dwordx4 v[170:171], v[174:177], off nt
	s_waitcnt lgkmcnt(0)
